# speedup vs baseline: 1.1407x; 1.0098x over previous
_Z6conv_kILi64ELi128ELi20ELi128ELi4ELi4ELb1EEvPKDF16_S1_PKfS3_PDF16_S4_S1_fS3_S3_S3_S3_:
	s_load_dwordx2 s[22:23], s[0:1], 0x8
	s_load_dwordx8 s[24:31], s[0:1], 0x40
	v_readfirstlane_b32 s34, v0
	s_lshr_b32 s35, s34, 6
	v_lshlrev_b32_e32 v1, 3, v0
	v_and_b32_e32 v2, 48, v0
	s_and_b32 s33, s2, 3
	v_bitop3_b32 v2, v1, v2, 56 bitop3:0x6c
	s_lshl_b32 s5, s35, 10
	v_and_b32_e32 v1, 0x1c0, v1
	s_and_b32 s4, s2, 56
	v_or3_b32 v18, s5, v1, v2
	v_and_b32_e32 v1, 7, v0
	s_mul_i32 s5, s33, 5
	v_or_b32_e32 v97, 0x200, v0
	s_lshl_b32 s3, s2, 3
	v_lshlrev_b32_e32 v19, 5, v1
	s_add_i32 s4, s4, s5
	v_mul_u32_u24_e32 v23, 0x283, v97
	s_and_b32 s3, s3, 32
	s_waitcnt lgkmcnt(0)
	global_load_dwordx4 v[2:5], v19, s[26:27] offset:16
	global_load_dwordx4 v[6:9], v19, s[28:29] offset:16
	global_load_dwordx4 v[10:13], v19, s[26:27]
	global_load_dwordx4 v[14:17], v19, s[28:29]
	s_add_i32 s20, s4, -9
	v_mul_u32_u24_e32 v19, 0xa1, v0
	s_movk_i32 s4, 0xffcd
	v_lshrrev_b32_e32 v23, 18, v23
	s_add_i32 s21, s3, -9
	v_lshrrev_b32_e32 v37, 3, v0
	v_mul_i32_i24_sdwa v20, v19, s4 dst_sel:DWORD dst_unused:UNUSED_PAD src0_sel:WORD_1 src1_sel:DWORD
	v_lshrrev_b32_e32 v50, 3, v97
	v_mul_i32_i24_e32 v24, 0xffffffcd, v23
	v_add_u32_sdwa v19, s20, v19 dst_sel:DWORD dst_unused:UNUSED_PAD src0_sel:DWORD src1_sel:WORD_1
	v_add3_u32 v20, s21, v37, v20
	v_add_u32_e32 v23, s20, v23
	v_add3_u32 v24, s21, v50, v24
	v_max_u32_e32 v21, v19, v20
	v_max_u32_e32 v25, v23, v24
	v_cmp_gt_u32_e64 s[16:17], 64, v21
	v_cmp_lt_u32_e64 s[14:15], 63, v25
	s_and_b32 s28, s2, 0xffffffc0
	v_cndmask_b32_e64 v19, 0, v19, s[16:17]
	v_cndmask_b32_e64 v23, v23, 0, s[14:15]
	v_or_b32_e32 v19, s28, v19
	v_cndmask_b32_e64 v20, 0, v20, s[16:17]
	v_or_b32_e32 v23, s28, v23
	v_cndmask_b32_e64 v24, v24, 0, s[14:15]
	v_lshl_add_u32 v20, v19, 6, v20
	v_cndmask_b32_e64 v19, 0, 1, s[16:17]
	v_lshl_add_u32 v24, v23, 6, v24
	v_cndmask_b32_e64 v23, 2, 0, s[14:15]
	v_or_b32_e32 v102, 0x400, v0
	v_or_b32_e32 v19, v23, v19
	v_mul_u32_u24_e32 v23, 0xa0b, v102
	v_lshrrev_b32_e32 v23, 20, v23
	v_lshrrev_b32_e32 v51, 3, v102
	v_mul_i32_i24_e32 v26, 0xffffffcd, v23
	v_add_u32_e32 v23, s20, v23
	v_add3_u32 v26, s21, v51, v26
	v_max_u32_e32 v27, v23, v26
	v_cmp_lt_u32_e64 s[12:13], 63, v27
	v_or_b32_e32 v103, 0x600, v0
	v_lshrrev_b32_e32 v52, 3, v103
	v_cndmask_b32_e64 v23, v23, 0, s[12:13]
	v_or_b32_e32 v23, s28, v23
	v_cndmask_b32_e64 v26, v26, 0, s[12:13]
	v_lshl_add_u32 v26, v23, 6, v26
	v_ashrrev_i32_e32 v27, 31, v26
	v_lshl_add_u64 v[38:39], v[26:27], 2, s[24:25]
	v_mul_u32_u24_e32 v26, 0xa0b, v103
	v_lshrrev_b32_e32 v26, 20, v26
	v_mul_i32_i24_e32 v27, 0xffffffcd, v26
	v_add_u32_e32 v26, s20, v26
	v_add3_u32 v27, s21, v52, v27
	v_max_u32_e32 v28, v26, v27
	v_cmp_lt_u32_e64 s[10:11], 63, v28
	v_cndmask_b32_e64 v23, 4, 0, s[12:13]
	v_or_b32_e32 v104, 0x800, v0
	v_cndmask_b32_e64 v26, v26, 0, s[10:11]
	v_or_b32_e32 v26, s28, v26
	v_cndmask_b32_e64 v27, v27, 0, s[10:11]
	v_lshl_add_u32 v26, v26, 6, v27
	v_ashrrev_i32_e32 v27, 31, v26
	v_lshl_add_u64 v[40:41], v[26:27], 2, s[24:25]
	v_cndmask_b32_e64 v26, 8, 0, s[10:11]
	v_or3_b32 v19, v19, v23, v26
	v_mul_u32_u24_e32 v23, 0x1415, v104
	v_lshrrev_b32_e32 v23, 21, v23
	v_lshrrev_b32_e32 v35, 3, v104
	v_mul_i32_i24_e32 v26, 0xffffffcd, v23
	v_add_u32_e32 v23, s20, v23
	v_add3_u32 v26, s21, v35, v26
	v_max_u32_e32 v27, v23, v26
	v_cmp_lt_u32_e64 s[8:9], 63, v27
	v_or_b32_e32 v105, 0xa00, v0
	v_lshrrev_b32_e32 v33, 3, v105
	v_cndmask_b32_e64 v23, v23, 0, s[8:9]
	v_or_b32_e32 v23, s28, v23
	v_cndmask_b32_e64 v26, v26, 0, s[8:9]
	v_lshl_add_u32 v26, v23, 6, v26
	v_ashrrev_i32_e32 v27, 31, v26
	v_lshl_add_u64 v[42:43], v[26:27], 2, s[24:25]
	v_mul_u32_u24_e32 v26, 0x1415, v105
	v_lshrrev_b32_e32 v26, 21, v26
	v_mul_i32_i24_e32 v27, 0xffffffcd, v26
	v_add_u32_e32 v26, s20, v26
	v_add3_u32 v27, s21, v33, v27
	v_max_u32_e32 v28, v26, v27
	v_cmp_lt_u32_e64 s[6:7], 63, v28
	v_cndmask_b32_e64 v23, 16, 0, s[8:9]
	v_or_b32_e32 v106, 0xc00, v0
	v_cndmask_b32_e64 v26, v26, 0, s[6:7]
	v_or_b32_e32 v26, s28, v26
	v_cndmask_b32_e64 v27, v27, 0, s[6:7]
	v_lshl_add_u32 v26, v26, 6, v27
	v_ashrrev_i32_e32 v27, 31, v26
	v_lshl_add_u64 v[44:45], v[26:27], 2, s[24:25]
	v_cndmask_b32_e64 v26, 32, 0, s[6:7]
	v_or3_b32 v30, v19, v23, v26
	v_mul_u32_u24_e32 v19, 0x1415, v106
	v_lshrrev_b32_e32 v19, 21, v19
	v_lshrrev_b32_e32 v31, 3, v106
	v_mul_i32_i24_e32 v23, 0xffffffcd, v19
	v_add_u32_e32 v19, s20, v19
	v_add3_u32 v23, s21, v31, v23
	v_max_u32_e32 v26, v19, v23
	v_cmp_gt_u32_e32 vcc, 64, v26
	v_or_b32_e32 v107, 0xe00, v0
	v_ashrrev_i32_e32 v21, 31, v20
	v_cndmask_b32_e32 v19, 0, v19, vcc
	v_or_b32_e32 v19, s28, v19
	v_cndmask_b32_e32 v23, 0, v23, vcc
	v_lshl_add_u32 v26, v19, 6, v23
	v_mul_u32_u24_e32 v23, 0x1415, v107
	v_ashrrev_i32_e32 v27, 31, v26
	v_lshrrev_b32_e32 v23, 21, v23
	v_lshl_add_u64 v[46:47], v[26:27], 2, s[24:25]
	v_lshrrev_b32_e32 v26, 3, v107
	v_mul_i32_i24_e32 v27, 0xffffffcd, v23
	v_add_u32_e32 v23, s20, v23
	v_add3_u32 v27, s21, v26, v27
	v_max_u32_e32 v28, v23, v27
	v_cndmask_b32_e64 v19, 0, 64, vcc
	v_cmp_gt_u32_e32 vcc, 64, v28
	v_lshl_add_u64 v[20:21], v[20:21], 2, s[24:25]
	v_ashrrev_i32_e32 v25, 31, v24
	v_cndmask_b32_e32 v23, 0, v23, vcc
	v_or_b32_e32 v23, s28, v23
	v_cndmask_b32_e32 v27, 0, v27, vcc
	v_lshl_add_u32 v28, v23, 6, v27
	v_ashrrev_i32_e32 v29, 31, v28
	s_load_dword s26, s[30:31], 0x0
	v_lshl_add_u64 v[24:25], v[24:25], 2, s[24:25]
	v_lshl_add_u64 v[48:49], v[28:29], 2, s[24:25]
	global_load_dword v53, v[20:21], off
	global_load_dword v54, v[24:25], off
	global_load_dword v55, v[38:39], off
	global_load_dword v56, v[40:41], off
	global_load_dword v57, v[42:43], off
	global_load_dword v36, v[44:45], off
	global_load_dword v34, v[46:47], off
	global_load_dword v29, v[48:49], off
	v_mov_b32_e32 v20, 0x80
	v_cndmask_b32_e32 v20, 0, v20, vcc
	v_or_b32_e32 v32, v19, v20
	v_or_b32_e32 v20, 0x1000, v0
	v_mul_u32_u24_e32 v21, 0x2829, v20
	v_lshrrev_b32_e32 v21, 22, v21
	v_lshrrev_b32_e32 v24, 3, v20
	v_mul_i32_i24_e32 v23, 0xffffffcd, v21
	v_add_u32_e32 v28, s20, v21
	s_movk_i32 s4, 0x1320
	v_add3_u32 v27, s21, v24, v23
	v_cmp_gt_u32_e64 s[4:5], s4, v20
	v_cmp_gt_u32_e32 vcc, 64, v28
	s_and_b64 s[18:19], s[4:5], vcc
	v_cmp_gt_u32_e32 vcc, 64, v27
	v_mov_b32_e32 v20, 0x100
	s_and_b64 s[18:19], s[18:19], vcc
	v_cndmask_b32_e64 v23, 0, v20, s[18:19]
	v_or_b32_e32 v20, 0x1200, v0
	v_lshrrev_b32_e32 v21, 3, v20
	v_mul_u32_u24_e32 v20, 0x2829, v20
	v_lshrrev_b32_e32 v20, 22, v20
	v_mul_i32_i24_e32 v25, 0xffffffcd, v20
	v_add_u32_e32 v20, s20, v20
	s_movk_i32 s20, 0x120
	v_add3_u32 v25, s21, v21, v25
	v_cmp_gt_u32_e32 vcc, s20, v0
	v_cmp_gt_u32_e64 s[20:21], 64, v20
	s_and_b64 s[30:31], vcc, s[20:21]
	v_cmp_gt_u32_e64 s[20:21], 64, v25
	s_and_b64 s[20:21], s[30:31], s[20:21]
	s_lshl_b32 s36, s35, 11
	v_cndmask_b32_e64 v20, 0, v20, s[20:21]
	v_or_b32_e32 v20, s28, v20
	v_cndmask_b32_e64 v25, 0, v25, s[20:21]
	v_lshl_add_u32 v38, v20, 6, v25
	v_mov_b32_e32 v25, 0x200
	v_or_b32_e32 v19, v32, v30
	v_ashrrev_i32_e32 v39, 31, v38
	v_cndmask_b32_e64 v25, 0, v25, s[20:21]
	s_add_i32 s27, s36, 0x14000
	s_mul_i32 s20, s33, 0x190000
	v_lshl_add_u64 v[38:39], v[38:39], 2, s[24:25]
	v_or3_b32 v25, v23, v25, v19
	v_mov_b32_e32 v19, 0
	s_add_u32 s20, s22, s20
	global_load_dword v20, v[38:39], off
	s_addc_u32 s21, s23, 0
	v_lshlrev_b64 v[38:39], 1, v[18:19]
	v_lshl_add_u64 v[40:41], s[20:21], 0, v[38:39]
	s_mov_b32 m0, s27
	s_mov_b64 s[30:31], 0x400
	global_load_lds_dwordx4 v[40:41], off
	s_add_i32 m0, s36, 0x14400
	v_lshl_add_u64 v[40:41], v[40:41], 0, s[30:31]
	s_add_u32 s30, s20, 0x50000
	s_addc_u32 s31, s21, 0
	global_load_lds_dwordx4 v[40:41], off
	s_add_i32 m0, s36, 0x18000
	v_lshl_add_u64 v[40:41], s[30:31], 0, v[38:39]
	v_or_b32_e32 v22, 0x200, v18
	v_mov_b32_e32 v23, v19
	global_load_lds_dwordx4 v[40:41], off
	s_add_i32 m0, s36, 0x18400
	v_lshlrev_b64 v[22:23], 1, v[22:23]
	s_add_u32 s20, s20, 0xa0000
	v_lshl_add_u64 v[40:41], s[30:31], 0, v[22:23]
	s_addc_u32 s21, s21, 0
	global_load_lds_dwordx4 v[40:41], off
	s_add_i32 m0, s36, 0x1c000
	v_lshl_add_u64 v[38:39], s[20:21], 0, v[38:39]
	global_load_lds_dwordx4 v[38:39], off
	v_lshl_add_u64 v[22:23], s[20:21], 0, v[22:23]
	s_add_i32 m0, s36, 0x1c400
	s_movk_i32 s29, 0x80
	global_load_lds_dwordx4 v[22:23], off
	s_waitcnt vmcnt(0)
	v_fma_f32 v22, v53, v10, v14
	s_waitcnt lgkmcnt(0)
	v_mul_f32_e32 v23, s26, v22
	v_cmp_le_f32_e64 s[20:21], 0, v22
	s_nop 1
	v_cndmask_b32_e64 v22, v23, v22, s[20:21]
	v_fma_f32 v23, v53, v11, v15
	v_mul_f32_e32 v38, s26, v23
	v_cmp_le_f32_e64 s[20:21], 0, v23
	v_cvt_f16_f32_e32 v22, v22
	v_cndmask_b32_e64 v22, 0, v22, s[16:17]
	v_cndmask_b32_e64 v23, v38, v23, s[20:21]
	v_fma_f32 v38, v53, v12, v16
	v_mul_f32_e32 v39, s26, v38
	v_cmp_le_f32_e64 s[20:21], 0, v38
	v_cvt_f16_f32_e32 v23, v23
	v_cndmask_b32_e64 v23, 0, v23, s[16:17]
	v_cndmask_b32_e64 v38, v39, v38, s[20:21]
	v_fma_f32 v39, v53, v13, v17
	v_mul_f32_e32 v40, s26, v39
	v_cmp_le_f32_e64 s[20:21], 0, v39
	v_cvt_f16_f32_e32 v38, v38
	v_cndmask_b32_e64 v38, 0, v38, s[16:17]
	v_cndmask_b32_e64 v39, v40, v39, s[20:21]
	v_fma_f32 v40, v53, v2, v6
	v_mul_f32_e32 v41, s26, v40
	v_cmp_le_f32_e64 s[20:21], 0, v40
	v_cvt_f16_f32_e32 v39, v39
	v_cndmask_b32_e64 v39, 0, v39, s[16:17]
	v_cndmask_b32_e64 v40, v41, v40, s[20:21]
	v_fma_f32 v41, v53, v3, v7
	v_mul_f32_e32 v42, s26, v41
	v_cmp_le_f32_e64 s[20:21], 0, v41
	v_cvt_f16_f32_e32 v40, v40
	v_pack_b32_f16 v39, v38, v39
	v_cndmask_b32_e64 v41, v42, v41, s[20:21]
	v_fma_f32 v42, v53, v4, v8
	v_mul_f32_e32 v43, s26, v42
	v_cmp_le_f32_e64 s[20:21], 0, v42
	v_cvt_f16_f32_e32 v41, v41
	v_pack_b32_f16 v38, v22, v23
	v_cndmask_b32_e64 v42, v43, v42, s[20:21]
	v_fma_f32 v43, v53, v5, v9
	v_mul_f32_e32 v44, s26, v43
	v_cmp_le_f32_e64 s[20:21], 0, v43
	v_cvt_f16_f32_e32 v42, v42
	v_bitop3_b32 v22, v37, v1, 6 bitop3:0x6c
	v_cndmask_b32_e64 v43, v44, v43, s[20:21]
	v_cvt_f16_f32_e32 v43, v43
	v_cndmask_b32_e64 v40, 0, v40, s[16:17]
	v_cndmask_b32_e64 v44, 0, v41, s[16:17]
	v_cndmask_b32_e64 v41, 0, v42, s[16:17]
	v_cndmask_b32_e64 v42, 0, v43, s[16:17]
	v_lshlrev_b32_e32 v22, 4, v22
	v_pack_b32_f16 v41, v41, v42
	v_pack_b32_f16 v40, v40, v44
	v_lshl_or_b32 v22, v37, 7, v22
	ds_write_b128 v22, v[38:41]
	v_fma_f32 v22, v54, v10, v14
	v_mul_f32_e32 v23, s26, v22
	v_cmp_le_f32_e64 s[16:17], 0, v22
	s_nop 1
	v_cndmask_b32_e64 v22, v23, v22, s[16:17]
	v_fma_f32 v23, v54, v11, v15
	v_mul_f32_e32 v37, s26, v23
	v_cmp_le_f32_e64 s[16:17], 0, v23
	v_cvt_f16_f32_e32 v22, v22
	v_cndmask_b32_e64 v22, v22, 0, s[14:15]
	v_cndmask_b32_e64 v23, v37, v23, s[16:17]
	v_fma_f32 v37, v54, v12, v16
	v_mul_f32_e32 v38, s26, v37
	v_cmp_le_f32_e64 s[16:17], 0, v37
	v_cvt_f16_f32_e32 v23, v23
	v_cndmask_b32_e64 v23, v23, 0, s[14:15]
	v_cndmask_b32_e64 v37, v38, v37, s[16:17]
	v_fma_f32 v38, v54, v13, v17
	v_mul_f32_e32 v39, s26, v38
	v_cmp_le_f32_e64 s[16:17], 0, v38
	v_cvt_f16_f32_e32 v37, v37
	v_cndmask_b32_e64 v37, v37, 0, s[14:15]
	v_cndmask_b32_e64 v38, v39, v38, s[16:17]
	v_fma_f32 v39, v54, v2, v6
	v_mul_f32_e32 v40, s26, v39
	v_cmp_le_f32_e64 s[16:17], 0, v39
	v_cvt_f16_f32_e32 v38, v38
	v_cndmask_b32_e64 v38, v38, 0, s[14:15]
	v_cndmask_b32_e64 v39, v40, v39, s[16:17]
	v_fma_f32 v40, v54, v3, v7
	v_mul_f32_e32 v41, s26, v40
	v_cmp_le_f32_e64 s[16:17], 0, v40
	v_cvt_f16_f32_e32 v39, v39
	v_cndmask_b32_e64 v39, v39, 0, s[14:15]
	v_cndmask_b32_e64 v40, v41, v40, s[16:17]
	v_fma_f32 v41, v54, v4, v8
	v_mul_f32_e32 v42, s26, v41
	v_cmp_le_f32_e64 s[16:17], 0, v41
	v_cvt_f16_f32_e32 v40, v40
	v_cndmask_b32_e64 v40, v40, 0, s[14:15]
	v_cndmask_b32_e64 v41, v42, v41, s[16:17]
	v_fma_f32 v42, v54, v5, v9
	v_mul_f32_e32 v43, s26, v42
	v_cmp_le_f32_e64 s[16:17], 0, v42
	v_cvt_f16_f32_e32 v41, v41
	v_pack_b32_f16 v40, v39, v40
	v_cndmask_b32_e64 v42, v43, v42, s[16:17]
	v_cvt_f16_f32_e32 v42, v42
	v_pack_b32_f16 v39, v37, v38
	v_pack_b32_f16 v38, v22, v23
	v_bitop3_b32 v22, v50, v1, 6 bitop3:0x6c
	v_cndmask_b32_e64 v41, v41, 0, s[14:15]
	v_cndmask_b32_e64 v42, v42, 0, s[14:15]
	v_lshlrev_b32_e32 v22, 4, v22
	v_pack_b32_f16 v41, v41, v42
	v_lshl_or_b32 v22, v50, 7, v22
	ds_write_b128 v22, v[38:41]
	v_fma_f32 v22, v55, v10, v14
	v_mul_f32_e32 v23, s26, v22
	v_cmp_le_f32_e64 s[14:15], 0, v22
	s_nop 1
	v_cndmask_b32_e64 v22, v23, v22, s[14:15]
	v_fma_f32 v23, v55, v11, v15
	v_mul_f32_e32 v37, s26, v23
	v_cmp_le_f32_e64 s[14:15], 0, v23
	v_cvt_f16_f32_e32 v22, v22
	v_cndmask_b32_e64 v22, v22, 0, s[12:13]
	v_cndmask_b32_e64 v23, v37, v23, s[14:15]
	v_fma_f32 v37, v55, v12, v16
	v_mul_f32_e32 v38, s26, v37
	v_cmp_le_f32_e64 s[14:15], 0, v37
	v_cvt_f16_f32_e32 v23, v23
	v_cndmask_b32_e64 v23, v23, 0, s[12:13]
	v_cndmask_b32_e64 v37, v38, v37, s[14:15]
	v_fma_f32 v38, v55, v13, v17
	v_mul_f32_e32 v39, s26, v38
	v_cmp_le_f32_e64 s[14:15], 0, v38
	v_cvt_f16_f32_e32 v37, v37
	v_cndmask_b32_e64 v37, v37, 0, s[12:13]
	v_cndmask_b32_e64 v38, v39, v38, s[14:15]
	v_fma_f32 v39, v55, v2, v6
	v_mul_f32_e32 v40, s26, v39
	v_cmp_le_f32_e64 s[14:15], 0, v39
	v_cvt_f16_f32_e32 v38, v38
	v_cndmask_b32_e64 v38, v38, 0, s[12:13]
	v_cndmask_b32_e64 v39, v40, v39, s[14:15]
	v_fma_f32 v40, v55, v3, v7
	v_mul_f32_e32 v41, s26, v40
	v_cmp_le_f32_e64 s[14:15], 0, v40
	v_cvt_f16_f32_e32 v39, v39
	v_cndmask_b32_e64 v39, v39, 0, s[12:13]
	v_cndmask_b32_e64 v40, v41, v40, s[14:15]
	v_fma_f32 v41, v55, v4, v8
	v_mul_f32_e32 v42, s26, v41
	v_cmp_le_f32_e64 s[14:15], 0, v41
	v_cvt_f16_f32_e32 v40, v40
	v_cndmask_b32_e64 v40, v40, 0, s[12:13]
	v_cndmask_b32_e64 v41, v42, v41, s[14:15]
	v_fma_f32 v42, v55, v5, v9
	v_mul_f32_e32 v43, s26, v42
	v_cmp_le_f32_e64 s[14:15], 0, v42
	v_cvt_f16_f32_e32 v41, v41
	v_pack_b32_f16 v40, v39, v40
	v_cndmask_b32_e64 v42, v43, v42, s[14:15]
	v_cvt_f16_f32_e32 v42, v42
	v_pack_b32_f16 v39, v37, v38
	v_pack_b32_f16 v38, v22, v23
	v_bitop3_b32 v22, v51, v1, 6 bitop3:0x6c
	v_cndmask_b32_e64 v41, v41, 0, s[12:13]
	v_cndmask_b32_e64 v42, v42, 0, s[12:13]
	v_lshlrev_b32_e32 v22, 4, v22
	v_pack_b32_f16 v41, v41, v42
	v_lshl_or_b32 v22, v51, 7, v22
	ds_write_b128 v22, v[38:41]
	v_fma_f32 v22, v56, v10, v14
	v_mul_f32_e32 v23, s26, v22
	v_cmp_le_f32_e64 s[12:13], 0, v22
	s_nop 1
	v_cndmask_b32_e64 v22, v23, v22, s[12:13]
	v_fma_f32 v23, v56, v11, v15
	v_mul_f32_e32 v37, s26, v23
	v_cmp_le_f32_e64 s[12:13], 0, v23
	v_cvt_f16_f32_e32 v22, v22
	v_cndmask_b32_e64 v22, v22, 0, s[10:11]
	v_cndmask_b32_e64 v23, v37, v23, s[12:13]
	v_fma_f32 v37, v56, v12, v16
	v_mul_f32_e32 v38, s26, v37
	v_cmp_le_f32_e64 s[12:13], 0, v37
	v_cvt_f16_f32_e32 v23, v23
	v_cndmask_b32_e64 v23, v23, 0, s[10:11]
	v_cndmask_b32_e64 v37, v38, v37, s[12:13]
	v_fma_f32 v38, v56, v13, v17
	v_mul_f32_e32 v39, s26, v38
	v_cmp_le_f32_e64 s[12:13], 0, v38
	v_cvt_f16_f32_e32 v37, v37
	v_cndmask_b32_e64 v37, v37, 0, s[10:11]
	v_cndmask_b32_e64 v38, v39, v38, s[12:13]
	v_fma_f32 v39, v56, v2, v6
	v_mul_f32_e32 v40, s26, v39
	v_cmp_le_f32_e64 s[12:13], 0, v39
	v_cvt_f16_f32_e32 v38, v38
	v_cndmask_b32_e64 v38, v38, 0, s[10:11]
	v_cndmask_b32_e64 v39, v40, v39, s[12:13]
	v_fma_f32 v40, v56, v3, v7
	v_mul_f32_e32 v41, s26, v40
	v_cmp_le_f32_e64 s[12:13], 0, v40
	v_cvt_f16_f32_e32 v39, v39
	v_cndmask_b32_e64 v39, v39, 0, s[10:11]
	v_cndmask_b32_e64 v40, v41, v40, s[12:13]
	v_fma_f32 v41, v56, v4, v8
	v_mul_f32_e32 v42, s26, v41
	v_cmp_le_f32_e64 s[12:13], 0, v41
	v_cvt_f16_f32_e32 v40, v40
	v_cndmask_b32_e64 v40, v40, 0, s[10:11]
	v_cndmask_b32_e64 v41, v42, v41, s[12:13]
	v_fma_f32 v42, v56, v5, v9
	v_mul_f32_e32 v43, s26, v42
	v_cmp_le_f32_e64 s[12:13], 0, v42
	v_cvt_f16_f32_e32 v41, v41
	v_pack_b32_f16 v40, v39, v40
	v_cndmask_b32_e64 v42, v43, v42, s[12:13]
	v_cvt_f16_f32_e32 v42, v42
	v_pack_b32_f16 v39, v37, v38
	v_pack_b32_f16 v38, v22, v23
	v_bitop3_b32 v22, v52, v1, 6 bitop3:0x6c
	v_cndmask_b32_e64 v41, v41, 0, s[10:11]
	v_cndmask_b32_e64 v42, v42, 0, s[10:11]
	v_lshlrev_b32_e32 v22, 4, v22
	v_pack_b32_f16 v41, v41, v42
	v_lshl_or_b32 v22, v52, 7, v22
	ds_write_b128 v22, v[38:41]
	v_fma_f32 v22, v57, v10, v14
	v_mul_f32_e32 v23, s26, v22
	v_cmp_le_f32_e64 s[10:11], 0, v22
	s_nop 1
	v_cndmask_b32_e64 v22, v23, v22, s[10:11]
	v_fma_f32 v23, v57, v11, v15
	v_mul_f32_e32 v37, s26, v23
	v_cmp_le_f32_e64 s[10:11], 0, v23
	v_cvt_f16_f32_e32 v22, v22
	v_cndmask_b32_e64 v22, v22, 0, s[8:9]
	v_cndmask_b32_e64 v23, v37, v23, s[10:11]
	v_fma_f32 v37, v57, v12, v16
	v_mul_f32_e32 v38, s26, v37
	v_cmp_le_f32_e64 s[10:11], 0, v37
	v_cvt_f16_f32_e32 v23, v23
	v_cndmask_b32_e64 v23, v23, 0, s[8:9]
	v_cndmask_b32_e64 v37, v38, v37, s[10:11]
	v_fma_f32 v38, v57, v13, v17
	v_mul_f32_e32 v39, s26, v38
	v_cmp_le_f32_e64 s[10:11], 0, v38
	v_cvt_f16_f32_e32 v37, v37
	v_cndmask_b32_e64 v37, v37, 0, s[8:9]
	v_cndmask_b32_e64 v38, v39, v38, s[10:11]
	v_fma_f32 v39, v57, v2, v6
	v_mul_f32_e32 v40, s26, v39
	v_cmp_le_f32_e64 s[10:11], 0, v39
	v_cvt_f16_f32_e32 v38, v38
	v_cndmask_b32_e64 v38, v38, 0, s[8:9]
	v_cndmask_b32_e64 v39, v40, v39, s[10:11]
	v_fma_f32 v40, v57, v3, v7
	v_mul_f32_e32 v41, s26, v40
	v_cmp_le_f32_e64 s[10:11], 0, v40
	v_cvt_f16_f32_e32 v39, v39
	v_cndmask_b32_e64 v39, v39, 0, s[8:9]
	v_cndmask_b32_e64 v40, v41, v40, s[10:11]
	v_fma_f32 v41, v57, v4, v8
	v_mul_f32_e32 v42, s26, v41
	v_cmp_le_f32_e64 s[10:11], 0, v41
	v_cvt_f16_f32_e32 v40, v40
	v_cndmask_b32_e64 v40, v40, 0, s[8:9]
	v_cndmask_b32_e64 v41, v42, v41, s[10:11]
	v_fma_f32 v42, v57, v5, v9
	v_mul_f32_e32 v43, s26, v42
	v_cmp_le_f32_e64 s[10:11], 0, v42
	v_cvt_f16_f32_e32 v41, v41
	v_pack_b32_f16 v40, v39, v40
	v_cndmask_b32_e64 v42, v43, v42, s[10:11]
	v_cvt_f16_f32_e32 v42, v42
	v_pack_b32_f16 v39, v37, v38
	v_pack_b32_f16 v38, v22, v23
	v_bitop3_b32 v22, v35, v1, 6 bitop3:0x6c
	v_cndmask_b32_e64 v41, v41, 0, s[8:9]
	v_cndmask_b32_e64 v42, v42, 0, s[8:9]
	v_lshlrev_b32_e32 v22, 4, v22
	v_pack_b32_f16 v41, v41, v42
	v_lshl_or_b32 v22, v35, 7, v22
	ds_write_b128 v22, v[38:41]
	v_fma_f32 v22, v36, v10, v14
	v_mul_f32_e32 v23, s26, v22
	v_cmp_le_f32_e64 s[8:9], 0, v22
	s_nop 1
	v_cndmask_b32_e64 v22, v23, v22, s[8:9]
	v_fma_f32 v23, v36, v11, v15
	v_mul_f32_e32 v35, s26, v23
	v_cmp_le_f32_e64 s[8:9], 0, v23
	v_cvt_f16_f32_e32 v22, v22
	v_cndmask_b32_e64 v22, v22, 0, s[6:7]
	v_cndmask_b32_e64 v23, v35, v23, s[8:9]
	v_fma_f32 v35, v36, v12, v16
	v_mul_f32_e32 v37, s26, v35
	v_cmp_le_f32_e64 s[8:9], 0, v35
	v_cvt_f16_f32_e32 v23, v23
	v_cndmask_b32_e64 v23, v23, 0, s[6:7]
	v_cndmask_b32_e64 v35, v37, v35, s[8:9]
	v_fma_f32 v37, v36, v13, v17
	v_mul_f32_e32 v38, s26, v37
	v_cmp_le_f32_e64 s[8:9], 0, v37
	v_cvt_f16_f32_e32 v35, v35
	v_cndmask_b32_e64 v35, v35, 0, s[6:7]
	v_cndmask_b32_e64 v37, v38, v37, s[8:9]
	v_fma_f32 v38, v36, v2, v6
	v_mul_f32_e32 v39, s26, v38
	v_cmp_le_f32_e64 s[8:9], 0, v38
	v_cvt_f16_f32_e32 v37, v37
	v_cndmask_b32_e64 v37, v37, 0, s[6:7]
	v_cndmask_b32_e64 v38, v39, v38, s[8:9]
	v_fma_f32 v39, v36, v3, v7
	v_mul_f32_e32 v40, s26, v39
	v_cmp_le_f32_e64 s[8:9], 0, v39
	v_cvt_f16_f32_e32 v38, v38
	v_pack_b32_f16 v37, v35, v37
	v_cndmask_b32_e64 v39, v40, v39, s[8:9]
	v_fma_f32 v40, v36, v4, v8
	v_mul_f32_e32 v41, s26, v40
	v_cmp_le_f32_e64 s[8:9], 0, v40
	v_fma_f32 v36, v36, v5, v9
	v_cvt_f16_f32_e32 v39, v39
	v_cndmask_b32_e64 v40, v41, v40, s[8:9]
	v_mul_f32_e32 v41, s26, v36
	v_cmp_le_f32_e64 s[8:9], 0, v36
	v_cvt_f16_f32_e32 v40, v40
	v_cndmask_b32_e64 v38, v38, 0, s[6:7]
	v_cndmask_b32_e64 v36, v41, v36, s[8:9]
	v_cvt_f16_f32_e32 v36, v36
	v_cndmask_b32_e64 v41, v39, 0, s[6:7]
	v_cndmask_b32_e64 v39, v40, 0, s[6:7]
	v_pack_b32_f16 v38, v38, v41
	v_cndmask_b32_e64 v36, v36, 0, s[6:7]
	v_pack_b32_f16 v39, v39, v36
	v_pack_b32_f16 v36, v22, v23
	v_bitop3_b32 v22, v33, v1, 6 bitop3:0x6c
	v_lshlrev_b32_e32 v22, 4, v22
	v_fma_f32 v23, v34, v10, v14
	v_lshl_or_b32 v22, v33, 7, v22
	v_mul_f32_e32 v33, s26, v23
	v_cmp_le_f32_e64 s[6:7], 0, v23
	ds_write_b128 v22, v[36:39]
	v_bitop3_b32 v22, v32, 64, v30 bitop3:0xc8
	v_cndmask_b32_e64 v23, v33, v23, s[6:7]
	v_fma_f32 v33, v34, v11, v15
	v_mul_f32_e32 v35, s26, v33
	v_cmp_le_f32_e64 s[6:7], 0, v33
	v_cvt_f16_f32_e32 v23, v23
	s_nop 0
	v_cndmask_b32_e64 v33, v35, v33, s[6:7]
	v_fma_f32 v35, v34, v12, v16
	v_mul_f32_e32 v36, s26, v35
	v_cmp_le_f32_e64 s[6:7], 0, v35
	v_cvt_f16_f32_e32 v33, v33
	s_nop 0
	v_cndmask_b32_e64 v35, v36, v35, s[6:7]
	v_fma_f32 v36, v34, v13, v17
	v_mul_f32_e32 v37, s26, v36
	v_cmp_le_f32_e64 s[6:7], 0, v36
	v_cvt_f16_f32_e32 v35, v35
	s_nop 0
	v_cndmask_b32_e64 v36, v37, v36, s[6:7]
	v_cvt_f16_f32_e32 v36, v36
	v_cmp_eq_u32_e64 s[6:7], 0, v22
	s_nop 1
	v_cndmask_b32_e64 v22, v23, 0, s[6:7]
	v_cndmask_b32_e64 v23, v33, 0, s[6:7]
	v_cndmask_b32_e64 v33, v35, 0, s[6:7]
	v_cndmask_b32_e64 v35, v36, 0, s[6:7]
	v_fma_f32 v36, v34, v2, v6
	v_mul_f32_e32 v37, s26, v36
	v_cmp_le_f32_e64 s[8:9], 0, v36
	v_pack_b32_f16 v35, v33, v35
	s_nop 0
	v_cndmask_b32_e64 v36, v37, v36, s[8:9]
	v_fma_f32 v37, v34, v3, v7
	v_mul_f32_e32 v38, s26, v37
	v_cmp_le_f32_e64 s[8:9], 0, v37
	v_cvt_f16_f32_e32 v36, v36
	v_cndmask_b32_e64 v36, v36, 0, s[6:7]
	v_cndmask_b32_e64 v37, v38, v37, s[8:9]
	v_fma_f32 v38, v34, v4, v8
	v_mul_f32_e32 v39, s26, v38
	v_cmp_le_f32_e64 s[8:9], 0, v38
	v_fma_f32 v34, v34, v5, v9
	v_cvt_f16_f32_e32 v37, v37
	v_cndmask_b32_e64 v38, v39, v38, s[8:9]
	v_mul_f32_e32 v39, s26, v34
	v_cmp_le_f32_e64 s[8:9], 0, v34
	v_cvt_f16_f32_e32 v38, v38
	s_nop 0
	v_cndmask_b32_e64 v34, v39, v34, s[8:9]
	v_cvt_f16_f32_e32 v34, v34
	v_cndmask_b32_e64 v39, v37, 0, s[6:7]
	v_cndmask_b32_e64 v37, v38, 0, s[6:7]
	v_pack_b32_f16 v36, v36, v39
	v_cndmask_b32_e64 v34, v34, 0, s[6:7]
	v_pack_b32_f16 v37, v37, v34
	v_pack_b32_f16 v34, v22, v23
	v_bitop3_b32 v22, v31, v1, 6 bitop3:0x6c
	v_lshlrev_b32_e32 v22, 4, v22
	v_lshl_or_b32 v22, v31, 7, v22
	v_fma_f32 v23, v29, v10, v14
	ds_write_b128 v22, v[34:37]
	v_bitop3_b32 v22, v32, s29, v30 bitop3:0xc8
	v_mul_f32_e32 v30, s26, v23
	v_cmp_le_f32_e64 s[6:7], 0, v23
	s_nop 1
	v_cndmask_b32_e64 v23, v30, v23, s[6:7]
	v_fma_f32 v30, v29, v11, v15
	v_mul_f32_e32 v31, s26, v30
	v_cmp_le_f32_e64 s[6:7], 0, v30
	v_cvt_f16_f32_e32 v23, v23
	s_nop 0
	v_cndmask_b32_e64 v30, v31, v30, s[6:7]
	v_fma_f32 v31, v29, v12, v16
	v_mul_f32_e32 v32, s26, v31
	v_cmp_le_f32_e64 s[6:7], 0, v31
	v_cvt_f16_f32_e32 v30, v30
	s_nop 0
	v_cndmask_b32_e64 v31, v32, v31, s[6:7]
	v_fma_f32 v32, v29, v13, v17
	v_mul_f32_e32 v33, s26, v32
	v_cmp_le_f32_e64 s[6:7], 0, v32
	v_cvt_f16_f32_e32 v31, v31
	s_nop 0
	v_cndmask_b32_e64 v32, v33, v32, s[6:7]
	v_cvt_f16_f32_e32 v32, v32
	v_cmp_eq_u32_e64 s[6:7], 0, v22
	s_nop 1
	v_cndmask_b32_e64 v22, v23, 0, s[6:7]
	v_cndmask_b32_e64 v23, v30, 0, s[6:7]
	v_cndmask_b32_e64 v30, v31, 0, s[6:7]
	v_cndmask_b32_e64 v31, v32, 0, s[6:7]
	v_fma_f32 v32, v29, v2, v6
	v_mul_f32_e32 v33, s26, v32
	v_cmp_le_f32_e64 s[8:9], 0, v32
	v_pack_b32_f16 v31, v30, v31
	v_pack_b32_f16 v30, v22, v23
	v_cndmask_b32_e64 v32, v33, v32, s[8:9]
	v_fma_f32 v33, v29, v3, v7
	v_mul_f32_e32 v34, s26, v33
	v_cmp_le_f32_e64 s[8:9], 0, v33
	v_cvt_f16_f32_e32 v32, v32
	v_bitop3_b32 v22, v26, v1, 6 bitop3:0x6c
	v_cndmask_b32_e64 v33, v34, v33, s[8:9]
	v_fma_f32 v34, v29, v4, v8
	v_mul_f32_e32 v35, s26, v34
	v_cmp_le_f32_e64 s[8:9], 0, v34
	v_fma_f32 v29, v29, v5, v9
	v_cvt_f16_f32_e32 v33, v33
	v_cndmask_b32_e64 v34, v35, v34, s[8:9]
	v_mul_f32_e32 v35, s26, v29
	v_cmp_le_f32_e64 s[8:9], 0, v29
	v_cvt_f16_f32_e32 v34, v34
	v_cndmask_b32_e64 v32, v32, 0, s[6:7]
	v_cndmask_b32_e64 v29, v35, v29, s[8:9]
	v_cvt_f16_f32_e32 v29, v29
	v_cndmask_b32_e64 v35, v33, 0, s[6:7]
	v_cndmask_b32_e64 v33, v34, 0, s[6:7]
	v_lshlrev_b32_e32 v22, 4, v22
	v_cndmask_b32_e64 v29, v29, 0, s[6:7]
	v_pack_b32_f16 v33, v33, v29
	v_pack_b32_f16 v32, v32, v35
	v_lshl_or_b32 v22, v26, 7, v22
	ds_write_b128 v22, v[30:33]
	s_and_saveexec_b64 s[6:7], s[4:5]
	s_cbranch_execz .LBB3_2
	v_cndmask_b32_e64 v22, 0, v28, s[18:19]
	v_or_b32_e32 v22, s28, v22
	v_cndmask_b32_e64 v23, 0, v27, s[18:19]
	v_lshl_add_u32 v22, v22, 6, v23
	v_ashrrev_i32_e32 v23, 31, v22
	v_lshl_add_u64 v[22:23], v[22:23], 2, s[24:25]
	global_load_dword v22, v[22:23], off
	v_bitop3_b32 v26, v24, v1, 6 bitop3:0x6c
	v_lshlrev_b32_e32 v30, 4, v26
	v_and_b32_e32 v23, 0x100, v25
	s_waitcnt vmcnt(0)
	v_fma_f32 v26, v22, v10, v14
	v_fma_f32 v27, v22, v11, v15
	v_mul_f32_e32 v34, s26, v26
	v_cmp_le_f32_e64 s[4:5], 0, v26
	v_fma_f32 v28, v22, v12, v16
	v_mul_f32_e32 v35, s26, v27
	v_cndmask_b32_e64 v26, v34, v26, s[4:5]
	v_cmp_le_f32_e64 s[4:5], 0, v27
	v_fma_f32 v29, v22, v13, v17
	v_mul_f32_e32 v36, s26, v28
	v_cndmask_b32_e64 v27, v35, v27, s[4:5]
	v_cmp_le_f32_e64 s[4:5], 0, v28
	v_fma_f32 v31, v22, v2, v6
	v_mul_f32_e32 v37, s26, v29
	v_cndmask_b32_e64 v28, v36, v28, s[4:5]
	v_cmp_le_f32_e64 s[4:5], 0, v29
	v_fma_f32 v32, v22, v3, v7
	v_mul_f32_e32 v38, s26, v31
	v_cndmask_b32_e64 v29, v37, v29, s[4:5]
	v_cmp_le_f32_e64 s[4:5], 0, v31
	v_fma_f32 v33, v22, v4, v8
	v_mul_f32_e32 v39, s26, v32
	v_cndmask_b32_e64 v31, v38, v31, s[4:5]
	v_cmp_le_f32_e64 s[4:5], 0, v32
	v_fma_f32 v22, v22, v5, v9
	v_mul_f32_e32 v40, s26, v33
	v_cndmask_b32_e64 v32, v39, v32, s[4:5]
	v_cmp_le_f32_e64 s[4:5], 0, v33
	v_mul_f32_e32 v41, s26, v22
	v_cvt_f16_f32_e32 v26, v26
	v_cndmask_b32_e64 v33, v40, v33, s[4:5]
	v_cmp_le_f32_e64 s[4:5], 0, v22
	v_cvt_f16_f32_e32 v27, v27
	v_cvt_f16_f32_e32 v28, v28
	v_cndmask_b32_e64 v22, v41, v22, s[4:5]
	v_cvt_f16_f32_e32 v29, v29
	v_cvt_f16_f32_e32 v31, v31
	v_cvt_f16_f32_e32 v32, v32
	v_cvt_f16_f32_e32 v33, v33
	v_cvt_f16_f32_e32 v22, v22
	v_cmp_eq_u32_e64 s[4:5], 0, v23
	s_nop 1
	v_cndmask_b32_e64 v23, v26, 0, s[4:5]
	v_cndmask_b32_e64 v26, v27, 0, s[4:5]
	v_cndmask_b32_e64 v27, v28, 0, s[4:5]
	v_cndmask_b32_e64 v34, v29, 0, s[4:5]
	v_cndmask_b32_e64 v28, v31, 0, s[4:5]
	v_cndmask_b32_e64 v31, v32, 0, s[4:5]
	v_cndmask_b32_e64 v29, v33, 0, s[4:5]
	v_cndmask_b32_e64 v22, v22, 0, s[4:5]
	v_pack_b32_f16 v29, v29, v22
	v_pack_b32_f16 v28, v28, v31
	v_pack_b32_f16 v27, v27, v34
	v_pack_b32_f16 v26, v23, v26
	v_lshl_or_b32 v22, v24, 7, v30
	ds_write_b128 v22, v[26:29]

.LBB3_4:
	s_or_b64 exec, exec, s[8:9]
	v_and_b32_e32 v96, 15, v0
	s_and_b32 s4, s35, 6
	v_mad_u64_u32 v[98:99], s[4:5], s4, 51, v[96:97]
	v_lshrrev_b32_e32 v108, 4, v0
	v_bfe_u32 v99, v0, 4, 2
	s_and_b32 s11, s34, 64
	v_and_b32_e32 v0, 6, v0
	v_or_b32_e32 v1, s11, v96
	v_bitop3_b32 v0, v108, v0, 3 bitop3:0x6c
	v_lshlrev_b32_e32 v1, 7, v1
	v_lshlrev_b32_e32 v0, 4, v0
	v_or_b32_e32 v2, v1, v0
	v_or_b32_e32 v110, 0x14000, v2
	s_mov_b32 s4, 0x14040
	s_waitcnt vmcnt(4) lgkmcnt(0)
	s_barrier
	ds_read_b128 v[40:43], v110
	v_bitop3_b32 v111, v1, s4, v0 bitop3:0x36
	ds_read_b128 v[48:51], v110 offset:2048
	v_lshlrev_b32_e32 v0, 7, v98
	v_bitop3_b32 v1, v98, v99, 6 bitop3:0x6c
	v_add_u32_e32 v109, 51, v98
	v_lshl_or_b32 v113, v1, 4, v0
	ds_read_b128 v[56:59], v113
	ds_read_b128 v[52:55], v113 offset:2048
	v_lshlrev_b32_e32 v0, 7, v109
	v_bitop3_b32 v1, v109, v99, 6 bitop3:0x6c
	v_lshl_or_b32 v114, v1, 4, v0
	ds_read_b128 v[64:67], v114
	ds_read_b128 v[68:71], v114 offset:2048
	ds_read_b128 v[76:79], v110 offset:4096
	ds_read_b128 v[80:83], v110 offset:6144
	v_mov_b32_e32 v92, 0
	s_lshr_b32 s10, s34, 7
	s_mul_i32 s12, s33, 0x64
	v_lshl_add_u64 v[100:101], v[18:19], 1, s[22:23]
	s_mov_b32 s5, 0
	s_mov_b32 s13, 0xc000
	s_mov_b64 s[8:9], 0x400
	v_mov_b32_e32 v112, 0x64
	s_mov_b32 s14, 0
	v_mov_b32_e32 v93, v92
	v_mov_b32_e32 v94, v92
	v_mov_b32_e32 v95, v92
	v_mov_b32_e32 v88, v92
	v_mov_b32_e32 v89, v92
	v_mov_b32_e32 v90, v92
	v_mov_b32_e32 v91, v92
	v_mov_b32_e32 v84, v92
	v_mov_b32_e32 v85, v92
	v_mov_b32_e32 v86, v92
	v_mov_b32_e32 v87, v92
	v_mov_b32_e32 v72, v92
	v_mov_b32_e32 v73, v92
	v_mov_b32_e32 v74, v92
	v_mov_b32_e32 v75, v92
	v_mov_b32_e32 v60, v92
	v_mov_b32_e32 v61, v92
	v_mov_b32_e32 v62, v92
	v_mov_b32_e32 v63, v92
	v_mov_b32_e32 v44, v92
	v_mov_b32_e32 v45, v92
	v_mov_b32_e32 v46, v92
	v_mov_b32_e32 v47, v92
	v_mov_b32_e32 v36, v92
	v_mov_b32_e32 v37, v92
	v_mov_b32_e32 v38, v92
	v_mov_b32_e32 v39, v92
	v_mov_b32_e32 v32, v92
	v_mov_b32_e32 v33, v92
	v_mov_b32_e32 v34, v92
	v_mov_b32_e32 v35, v92
	v_mov_b32_e32 v28, v92
	v_mov_b32_e32 v29, v92
	v_mov_b32_e32 v30, v92
	v_mov_b32_e32 v31, v92
	v_mov_b32_e32 v24, v92
	v_mov_b32_e32 v25, v92
	v_mov_b32_e32 v26, v92
	v_mov_b32_e32 v27, v92
	v_mov_b32_e32 v20, v92
	v_mov_b32_e32 v21, v92
	v_mov_b32_e32 v22, v92
	v_mov_b32_e32 v23, v92
	v_mov_b32_e32 v16, v92
	v_mov_b32_e32 v17, v92
	v_mov_b32_e32 v18, v92
	v_mov_b32_e32 v19, v92
	v_mov_b32_e32 v12, v92
	v_mov_b32_e32 v13, v92
	v_mov_b32_e32 v14, v92
	v_mov_b32_e32 v15, v92
	v_mov_b32_e32 v8, v92
	v_mov_b32_e32 v9, v92
	v_mov_b32_e32 v10, v92
	v_mov_b32_e32 v11, v92
	v_mov_b32_e32 v4, v92
	v_mov_b32_e32 v5, v92
	v_mov_b32_e32 v6, v92
	v_mov_b32_e32 v7, v92
	v_mov_b32_e32 v0, v92
	v_mov_b32_e32 v1, v92
	v_mov_b32_e32 v2, v92
	v_mov_b32_e32 v3, v92
	s_mov_b32 s40, 1
	s_mov_b32 s41, 1
	v_mov_b32_e32 v115, v111
	s_add_i32 s4, s12, 3
	s_lshl_b32 s4, s4, 14
	v_lshl_add_u64 v[148:149], v[100:101], 0, s[4:5]
	s_add_i32 s42, s27, 0xc000
	v_lshl_add_u64 v[150:151], v[148:149], 0, s[8:9]
	s_mov_b32 s45, 0
	s_waitcnt lgkmcnt(0)
.Lc1_loop:
	s_waitcnt vmcnt(2)
	s_barrier
	s_waitcnt lgkmcnt(3)
	v_mfma_f32_16x16x32_f16 v[92:95], v[40:43], v[56:59], v[92:95]
	ds_read_b128 v[116:119], v115
	v_mfma_f32_16x16x32_f16 v[88:91], v[48:51], v[56:59], v[88:91]
	v_xor_b32_e32 v153, 64, v114
	s_add_i32 s4, s45, 60
	s_add_i32 s4, s4, s12
	s_lshl_b32 s4, s4, 14
	s_waitcnt lgkmcnt(3)
	v_mfma_f32_16x16x32_f16 v[60:63], v[40:43], v[52:55], v[60:63]
	ds_read_b128 v[120:123], v115 offset:2048
	v_lshl_add_u64 v[148:149], v[100:101], 0, s[4:5]
	s_and_b32 s42, s13, 0xc000
	s_add_i32 s42, s42, s27
	v_mfma_f32_16x16x32_f16 v[44:47], v[48:51], v[52:55], v[44:47]
	v_xor_b32_e32 v152, 64, v113
	s_mov_b32 m0, s42
	s_add_i32 s16, s13, 0xffff8000
	global_load_lds_dwordx4 v[148:149], off
	v_mfma_f32_16x16x32_f16 v[28:31], v[40:43], v[64:67], v[28:31]
	ds_read_b128 v[132:135], v153
	v_mfma_f32_16x16x32_f16 v[24:27], v[48:51], v[64:67], v[24:27]
	s_and_b32 s16, s16, 0xc000
	s_add_i32 s43, s42, 0x400
	v_lshl_add_u64 v[150:151], v[148:149], 0, s[8:9]
	v_mfma_f32_16x16x32_f16 v[12:15], v[40:43], v[68:71], v[12:15]
	ds_read_b128 v[136:139], v153 offset:2048
	v_mfma_f32_16x16x32_f16 v[8:11], v[48:51], v[68:71], v[8:11]
	v_add_u32_e32 v154, s16, v110
	s_add_i32 s44, s45, 102
	s_waitcnt lgkmcnt(5)
	v_mfma_f32_16x16x32_f16 v[84:87], v[76:79], v[56:59], v[84:87]
	ds_read_b128 v[124:127], v152
	s_waitcnt lgkmcnt(5)
	v_mfma_f32_16x16x32_f16 v[72:75], v[80:83], v[56:59], v[72:75]
	v_mfma_f32_16x16x32_f16 v[36:39], v[76:79], v[52:55], v[36:39]
	ds_read_b128 v[128:131], v152 offset:2048
	v_mfma_f32_16x16x32_f16 v[32:35], v[80:83], v[52:55], v[32:35]
	v_add_u32_e32 v155, s44, v98
	v_mfma_f32_16x16x32_f16 v[20:23], v[76:79], v[64:67], v[20:23]
	ds_read_b128 v[140:143], v115 offset:4096
	v_mfma_f32_16x16x32_f16 v[16:19], v[80:83], v[64:67], v[16:19]
	v_lshlrev_b32_e32 v156, 7, v155
	v_bitop3_b32 v155, v155, v99, 6 bitop3:0x6c
	v_mfma_f32_16x16x32_f16 v[4:7], v[76:79], v[68:71], v[4:7]
	ds_read_b128 v[144:147], v115 offset:6144
	v_mfma_f32_16x16x32_f16 v[0:3], v[80:83], v[68:71], v[0:3]
	v_lshl_or_b32 v114, v155, 4, v156
	v_add_u32_e32 v115, s16, v111
	s_waitcnt lgkmcnt(3)
	v_mfma_f32_16x16x32_f16 v[92:95], v[116:119], v[124:127], v[92:95]
	ds_read_b128 v[40:43], v154
	v_mfma_f32_16x16x32_f16 v[88:91], v[120:123], v[124:127], v[88:91]
	s_mov_b32 m0, s43
	s_addk_i32 s13, 0x4000
	global_load_lds_dwordx4 v[150:151], off
	s_waitcnt lgkmcnt(3)
	v_mfma_f32_16x16x32_f16 v[60:63], v[116:119], v[128:131], v[60:63]
	ds_read_b128 v[48:51], v154 offset:2048
	v_mfma_f32_16x16x32_f16 v[44:47], v[120:123], v[128:131], v[44:47]
	v_mfma_f32_16x16x32_f16 v[28:31], v[116:119], v[132:135], v[28:31]
	ds_read_b128 v[56:59], v114
	v_mfma_f32_16x16x32_f16 v[24:27], v[120:123], v[132:135], v[24:27]
	v_mfma_f32_16x16x32_f16 v[12:15], v[116:119], v[136:139], v[12:15]
	ds_read_b128 v[52:55], v114 offset:2048
	v_mfma_f32_16x16x32_f16 v[8:11], v[120:123], v[136:139], v[8:11]
	s_waitcnt lgkmcnt(5)
	v_mfma_f32_16x16x32_f16 v[84:87], v[140:143], v[124:127], v[84:87]
	s_waitcnt lgkmcnt(4)
	v_mfma_f32_16x16x32_f16 v[72:75], v[144:147], v[124:127], v[72:75]
	v_mfma_f32_16x16x32_f16 v[36:39], v[140:143], v[128:131], v[36:39]
	v_mfma_f32_16x16x32_f16 v[32:35], v[144:147], v[128:131], v[32:35]
	v_mfma_f32_16x16x32_f16 v[20:23], v[140:143], v[132:135], v[20:23]
	ds_read_b128 v[76:79], v154 offset:4096
	v_mfma_f32_16x16x32_f16 v[16:19], v[144:147], v[132:135], v[16:19]
	v_mfma_f32_16x16x32_f16 v[4:7], v[140:143], v[136:139], v[4:7]
	ds_read_b128 v[80:83], v154 offset:6144
	v_mfma_f32_16x16x32_f16 v[0:3], v[144:147], v[136:139], v[0:3]
	s_waitcnt vmcnt(2)
	s_barrier
	s_waitcnt lgkmcnt(5)
	v_mfma_f32_16x16x32_f16 v[92:95], v[40:43], v[64:67], v[92:95]
	ds_read_b128 v[116:119], v115
	s_waitcnt lgkmcnt(5)
	v_mfma_f32_16x16x32_f16 v[88:91], v[48:51], v[64:67], v[88:91]
	v_xor_b32_e32 v153, 64, v114
	s_add_i32 s4, s45, 80
	s_add_i32 s4, s4, s12
	s_lshl_b32 s4, s4, 14
	v_mfma_f32_16x16x32_f16 v[60:63], v[40:43], v[68:71], v[60:63]
	ds_read_b128 v[120:123], v115 offset:2048
	v_lshl_add_u64 v[148:149], v[100:101], 0, s[4:5]
	s_and_b32 s42, s13, 0xc000
	s_add_i32 s42, s42, s27
	v_mfma_f32_16x16x32_f16 v[44:47], v[48:51], v[68:71], v[44:47]
	s_mov_b32 m0, s42
	s_add_i32 s16, s13, 0xffff8000
	global_load_lds_dwordx4 v[148:149], off
	s_waitcnt lgkmcnt(5)
	v_mfma_f32_16x16x32_f16 v[28:31], v[40:43], v[56:59], v[28:31]
	ds_read_b128 v[124:127], v153
	v_mfma_f32_16x16x32_f16 v[24:27], v[48:51], v[56:59], v[24:27]
	s_and_b32 s16, s16, 0xc000
	s_add_i32 s43, s42, 0x400
	v_lshl_add_u64 v[150:151], v[148:149], 0, s[8:9]
	s_waitcnt lgkmcnt(5)
	v_mfma_f32_16x16x32_f16 v[12:15], v[40:43], v[52:55], v[12:15]
	ds_read_b128 v[128:131], v153 offset:2048
	v_mfma_f32_16x16x32_f16 v[8:11], v[48:51], v[52:55], v[8:11]
	v_add_u32_e32 v154, s16, v110
	s_add_i32 s44, s45, 153
	s_waitcnt lgkmcnt(5)
	v_mfma_f32_16x16x32_f16 v[84:87], v[76:79], v[64:67], v[84:87]
	s_waitcnt lgkmcnt(4)
	v_mfma_f32_16x16x32_f16 v[72:75], v[80:83], v[64:67], v[72:75]
	v_mfma_f32_16x16x32_f16 v[36:39], v[76:79], v[68:71], v[36:39]
	v_mfma_f32_16x16x32_f16 v[32:35], v[80:83], v[68:71], v[32:35]
	v_add_u32_e32 v155, s44, v98
	v_mfma_f32_16x16x32_f16 v[20:23], v[76:79], v[56:59], v[20:23]
	ds_read_b128 v[140:143], v115 offset:4096
	v_mfma_f32_16x16x32_f16 v[16:19], v[80:83], v[56:59], v[16:19]
	v_lshlrev_b32_e32 v156, 7, v155
	v_bitop3_b32 v155, v155, v99, 6 bitop3:0x6c
	v_mfma_f32_16x16x32_f16 v[4:7], v[76:79], v[52:55], v[4:7]
	ds_read_b128 v[144:147], v115 offset:6144
	v_mfma_f32_16x16x32_f16 v[0:3], v[80:83], v[52:55], v[0:3]
	v_lshl_or_b32 v114, v155, 4, v156
	v_add_u32_e32 v115, s16, v111
	s_waitcnt lgkmcnt(5)
	v_mfma_f32_16x16x32_f16 v[92:95], v[116:119], v[132:135], v[92:95]
	ds_read_b128 v[40:43], v154
	s_waitcnt lgkmcnt(5)
	v_mfma_f32_16x16x32_f16 v[88:91], v[120:123], v[132:135], v[88:91]
	s_mov_b32 m0, s43
	s_addk_i32 s13, 0x4000
	global_load_lds_dwordx4 v[150:151], off
	v_mfma_f32_16x16x32_f16 v[60:63], v[116:119], v[136:139], v[60:63]
	ds_read_b128 v[48:51], v154 offset:2048
	v_mfma_f32_16x16x32_f16 v[44:47], v[120:123], v[136:139], v[44:47]
	s_waitcnt lgkmcnt(5)
	v_mfma_f32_16x16x32_f16 v[28:31], v[116:119], v[124:127], v[28:31]
	ds_read_b128 v[64:67], v114
	v_mfma_f32_16x16x32_f16 v[24:27], v[120:123], v[124:127], v[24:27]
	s_waitcnt lgkmcnt(5)
	v_mfma_f32_16x16x32_f16 v[12:15], v[116:119], v[128:131], v[12:15]
	ds_read_b128 v[68:71], v114 offset:2048
	v_mfma_f32_16x16x32_f16 v[8:11], v[120:123], v[128:131], v[8:11]
	s_waitcnt lgkmcnt(5)
	v_mfma_f32_16x16x32_f16 v[84:87], v[140:143], v[132:135], v[84:87]
	s_waitcnt lgkmcnt(4)
	v_mfma_f32_16x16x32_f16 v[72:75], v[144:147], v[132:135], v[72:75]
	v_mfma_f32_16x16x32_f16 v[36:39], v[140:143], v[136:139], v[36:39]
	v_mfma_f32_16x16x32_f16 v[32:35], v[144:147], v[136:139], v[32:35]
	v_mfma_f32_16x16x32_f16 v[20:23], v[140:143], v[124:127], v[20:23]
	ds_read_b128 v[76:79], v154 offset:4096
	v_mfma_f32_16x16x32_f16 v[16:19], v[144:147], v[124:127], v[16:19]
	v_mfma_f32_16x16x32_f16 v[4:7], v[140:143], v[128:131], v[4:7]
	ds_read_b128 v[80:83], v154 offset:6144
	v_mfma_f32_16x16x32_f16 v[0:3], v[144:147], v[128:131], v[0:3]
	s_waitcnt vmcnt(2)
	s_barrier
	s_waitcnt lgkmcnt(5)
	v_mfma_f32_16x16x32_f16 v[92:95], v[40:43], v[56:59], v[92:95]
	ds_read_b128 v[116:119], v115
	s_waitcnt lgkmcnt(5)
	v_mfma_f32_16x16x32_f16 v[88:91], v[48:51], v[56:59], v[88:91]
	v_xor_b32_e32 v153, 64, v114
	s_add_i32 s4, s45, 1
	s_add_i32 s4, s4, s12
	s_lshl_b32 s4, s4, 14
	v_mfma_f32_16x16x32_f16 v[60:63], v[40:43], v[52:55], v[60:63]
	ds_read_b128 v[120:123], v115 offset:2048
	v_lshl_add_u64 v[148:149], v[100:101], 0, s[4:5]
	s_and_b32 s42, s13, 0xc000
	s_add_i32 s42, s42, s27
	v_mfma_f32_16x16x32_f16 v[44:47], v[48:51], v[52:55], v[44:47]
	s_mov_b32 m0, s42
	s_add_i32 s16, s13, 0xffff8000
	global_load_lds_dwordx4 v[148:149], off
	s_waitcnt lgkmcnt(5)
	v_mfma_f32_16x16x32_f16 v[28:31], v[40:43], v[64:67], v[28:31]
	ds_read_b128 v[132:135], v153
	v_mfma_f32_16x16x32_f16 v[24:27], v[48:51], v[64:67], v[24:27]
	s_and_b32 s16, s16, 0xc000
	s_add_i32 s43, s42, 0x400
	v_lshl_add_u64 v[150:151], v[148:149], 0, s[8:9]
	s_waitcnt lgkmcnt(5)
	v_mfma_f32_16x16x32_f16 v[12:15], v[40:43], v[68:71], v[12:15]
	ds_read_b128 v[136:139], v153 offset:2048
	v_mfma_f32_16x16x32_f16 v[8:11], v[48:51], v[68:71], v[8:11]
	v_add_u32_e32 v154, s16, v110
	s_add_i32 s44, s45, 204
	s_waitcnt lgkmcnt(5)
	v_mfma_f32_16x16x32_f16 v[84:87], v[76:79], v[56:59], v[84:87]
	s_waitcnt lgkmcnt(4)
	v_mfma_f32_16x16x32_f16 v[72:75], v[80:83], v[56:59], v[72:75]
	v_mfma_f32_16x16x32_f16 v[36:39], v[76:79], v[52:55], v[36:39]
	v_mfma_f32_16x16x32_f16 v[32:35], v[80:83], v[52:55], v[32:35]
	v_add_u32_e32 v155, s44, v98
	v_mfma_f32_16x16x32_f16 v[20:23], v[76:79], v[64:67], v[20:23]
	ds_read_b128 v[140:143], v115 offset:4096
	v_mfma_f32_16x16x32_f16 v[16:19], v[80:83], v[64:67], v[16:19]
	v_lshlrev_b32_e32 v156, 7, v155
	v_bitop3_b32 v155, v155, v99, 6 bitop3:0x6c
	v_mfma_f32_16x16x32_f16 v[4:7], v[76:79], v[68:71], v[4:7]
	ds_read_b128 v[144:147], v115 offset:6144
	v_mfma_f32_16x16x32_f16 v[0:3], v[80:83], v[68:71], v[0:3]
	v_lshl_or_b32 v114, v155, 4, v156
	v_add_u32_e32 v115, s16, v111
	s_waitcnt lgkmcnt(5)
	v_mfma_f32_16x16x32_f16 v[92:95], v[116:119], v[124:127], v[92:95]
	ds_read_b128 v[40:43], v154
	s_waitcnt lgkmcnt(5)
	v_mfma_f32_16x16x32_f16 v[88:91], v[120:123], v[124:127], v[88:91]
	s_mov_b32 m0, s43
	s_addk_i32 s13, 0x4000
	global_load_lds_dwordx4 v[150:151], off
	v_mfma_f32_16x16x32_f16 v[60:63], v[116:119], v[128:131], v[60:63]
	ds_read_b128 v[48:51], v154 offset:2048
	v_mfma_f32_16x16x32_f16 v[44:47], v[120:123], v[128:131], v[44:47]
	s_waitcnt lgkmcnt(5)
	v_mfma_f32_16x16x32_f16 v[28:31], v[116:119], v[132:135], v[28:31]
	ds_read_b128 v[56:59], v114
	v_mfma_f32_16x16x32_f16 v[24:27], v[120:123], v[132:135], v[24:27]
	s_waitcnt lgkmcnt(5)
	v_mfma_f32_16x16x32_f16 v[12:15], v[116:119], v[136:139], v[12:15]
	ds_read_b128 v[52:55], v114 offset:2048
	v_mfma_f32_16x16x32_f16 v[8:11], v[120:123], v[136:139], v[8:11]
	s_waitcnt lgkmcnt(5)
	v_mfma_f32_16x16x32_f16 v[84:87], v[140:143], v[124:127], v[84:87]
	s_waitcnt lgkmcnt(4)
	v_mfma_f32_16x16x32_f16 v[72:75], v[144:147], v[124:127], v[72:75]
	v_mfma_f32_16x16x32_f16 v[36:39], v[140:143], v[128:131], v[36:39]
	v_mfma_f32_16x16x32_f16 v[32:35], v[144:147], v[128:131], v[32:35]
	v_mfma_f32_16x16x32_f16 v[20:23], v[140:143], v[132:135], v[20:23]
	ds_read_b128 v[76:79], v154 offset:4096
	v_mfma_f32_16x16x32_f16 v[16:19], v[144:147], v[132:135], v[16:19]
	v_mfma_f32_16x16x32_f16 v[4:7], v[140:143], v[136:139], v[4:7]
	ds_read_b128 v[80:83], v154 offset:6144
	v_mfma_f32_16x16x32_f16 v[0:3], v[144:147], v[136:139], v[0:3]
	s_waitcnt vmcnt(2)
	s_barrier
	s_waitcnt lgkmcnt(5)
	v_mfma_f32_16x16x32_f16 v[92:95], v[40:43], v[64:67], v[92:95]
	ds_read_b128 v[116:119], v115
	s_waitcnt lgkmcnt(5)
	v_mfma_f32_16x16x32_f16 v[88:91], v[48:51], v[64:67], v[88:91]
	v_xor_b32_e32 v153, 64, v114
	s_add_i32 s4, s45, 21
	s_add_i32 s4, s4, s12
	s_lshl_b32 s4, s4, 14
	v_mfma_f32_16x16x32_f16 v[60:63], v[40:43], v[68:71], v[60:63]
	ds_read_b128 v[120:123], v115 offset:2048
	v_lshl_add_u64 v[148:149], v[100:101], 0, s[4:5]
	s_and_b32 s42, s13, 0xc000
	s_add_i32 s42, s42, s27
	v_mfma_f32_16x16x32_f16 v[44:47], v[48:51], v[68:71], v[44:47]
	s_mov_b32 m0, s42
	s_add_i32 s16, s13, 0xffff8000
	global_load_lds_dwordx4 v[148:149], off
	s_waitcnt lgkmcnt(5)
	v_mfma_f32_16x16x32_f16 v[28:31], v[40:43], v[56:59], v[28:31]
	ds_read_b128 v[124:127], v153
	v_mfma_f32_16x16x32_f16 v[24:27], v[48:51], v[56:59], v[24:27]
	s_and_b32 s16, s16, 0xc000
	s_add_i32 s43, s42, 0x400
	v_lshl_add_u64 v[150:151], v[148:149], 0, s[8:9]
	s_waitcnt lgkmcnt(5)
	v_mfma_f32_16x16x32_f16 v[12:15], v[40:43], v[52:55], v[12:15]
	ds_read_b128 v[128:131], v153 offset:2048
	v_mfma_f32_16x16x32_f16 v[8:11], v[48:51], v[52:55], v[8:11]
	v_add_u32_e32 v154, s16, v110
	s_add_i32 s44, s45, 255
	s_waitcnt lgkmcnt(5)
	v_mfma_f32_16x16x32_f16 v[84:87], v[76:79], v[64:67], v[84:87]
	s_waitcnt lgkmcnt(4)
	v_mfma_f32_16x16x32_f16 v[72:75], v[80:83], v[64:67], v[72:75]
	v_mfma_f32_16x16x32_f16 v[36:39], v[76:79], v[68:71], v[36:39]
	v_mfma_f32_16x16x32_f16 v[32:35], v[80:83], v[68:71], v[32:35]
	v_add_u32_e32 v155, s44, v98
	v_mfma_f32_16x16x32_f16 v[20:23], v[76:79], v[56:59], v[20:23]
	ds_read_b128 v[140:143], v115 offset:4096
	v_mfma_f32_16x16x32_f16 v[16:19], v[80:83], v[56:59], v[16:19]
	v_lshlrev_b32_e32 v156, 7, v155
	v_bitop3_b32 v155, v155, v99, 6 bitop3:0x6c
	v_mfma_f32_16x16x32_f16 v[4:7], v[76:79], v[52:55], v[4:7]
	ds_read_b128 v[144:147], v115 offset:6144
	v_mfma_f32_16x16x32_f16 v[0:3], v[80:83], v[52:55], v[0:3]
	v_lshl_or_b32 v114, v155, 4, v156
	v_add_u32_e32 v115, s16, v111
	s_waitcnt lgkmcnt(5)
	v_mfma_f32_16x16x32_f16 v[92:95], v[116:119], v[132:135], v[92:95]
	ds_read_b128 v[40:43], v154
	s_waitcnt lgkmcnt(5)
	v_mfma_f32_16x16x32_f16 v[88:91], v[120:123], v[132:135], v[88:91]
	s_mov_b32 m0, s43
	s_addk_i32 s13, 0x4000
	global_load_lds_dwordx4 v[150:151], off
	v_mfma_f32_16x16x32_f16 v[60:63], v[116:119], v[136:139], v[60:63]
	ds_read_b128 v[48:51], v154 offset:2048
	v_mfma_f32_16x16x32_f16 v[44:47], v[120:123], v[136:139], v[44:47]
	s_waitcnt lgkmcnt(5)
	v_mfma_f32_16x16x32_f16 v[28:31], v[116:119], v[124:127], v[28:31]
	ds_read_b128 v[64:67], v114
	v_mfma_f32_16x16x32_f16 v[24:27], v[120:123], v[124:127], v[24:27]
	s_waitcnt lgkmcnt(5)
	v_mfma_f32_16x16x32_f16 v[12:15], v[116:119], v[128:131], v[12:15]
	ds_read_b128 v[68:71], v114 offset:2048
	v_mfma_f32_16x16x32_f16 v[8:11], v[120:123], v[128:131], v[8:11]
	s_waitcnt lgkmcnt(5)
	v_mfma_f32_16x16x32_f16 v[84:87], v[140:143], v[132:135], v[84:87]
	s_waitcnt lgkmcnt(4)
	v_mfma_f32_16x16x32_f16 v[72:75], v[144:147], v[132:135], v[72:75]
	v_mfma_f32_16x16x32_f16 v[36:39], v[140:143], v[136:139], v[36:39]
	v_mfma_f32_16x16x32_f16 v[32:35], v[144:147], v[136:139], v[32:35]
	v_mfma_f32_16x16x32_f16 v[20:23], v[140:143], v[124:127], v[20:23]
	ds_read_b128 v[76:79], v154 offset:4096
	v_mfma_f32_16x16x32_f16 v[16:19], v[144:147], v[124:127], v[16:19]
	v_mfma_f32_16x16x32_f16 v[4:7], v[140:143], v[128:131], v[4:7]
	ds_read_b128 v[80:83], v154 offset:6144
	v_mfma_f32_16x16x32_f16 v[0:3], v[144:147], v[128:131], v[0:3]
	s_waitcnt vmcnt(2)
	s_barrier
	s_waitcnt lgkmcnt(5)
	v_mfma_f32_16x16x32_f16 v[92:95], v[40:43], v[56:59], v[92:95]
	ds_read_b128 v[116:119], v115
	s_waitcnt lgkmcnt(5)
	v_mfma_f32_16x16x32_f16 v[88:91], v[48:51], v[56:59], v[88:91]
	v_xor_b32_e32 v153, 64, v114
	s_add_i32 s4, s45, 41
	s_add_i32 s4, s4, s12
	s_lshl_b32 s4, s4, 14
	v_mfma_f32_16x16x32_f16 v[60:63], v[40:43], v[52:55], v[60:63]
	ds_read_b128 v[120:123], v115 offset:2048
	v_lshl_add_u64 v[148:149], v[100:101], 0, s[4:5]
	s_and_b32 s42, s13, 0xc000
	s_add_i32 s42, s42, s27
	v_mfma_f32_16x16x32_f16 v[44:47], v[48:51], v[52:55], v[44:47]
	s_mov_b32 m0, s42
	s_add_i32 s16, s13, 0xffff8000
	global_load_lds_dwordx4 v[148:149], off
	s_waitcnt lgkmcnt(5)
	v_mfma_f32_16x16x32_f16 v[28:31], v[40:43], v[64:67], v[28:31]
	ds_read_b128 v[132:135], v153
	v_mfma_f32_16x16x32_f16 v[24:27], v[48:51], v[64:67], v[24:27]
	s_and_b32 s16, s16, 0xc000
	s_add_i32 s43, s42, 0x400
	v_lshl_add_u64 v[150:151], v[148:149], 0, s[8:9]
	s_waitcnt lgkmcnt(5)
	v_mfma_f32_16x16x32_f16 v[12:15], v[40:43], v[68:71], v[12:15]
	ds_read_b128 v[136:139], v153 offset:2048
	v_mfma_f32_16x16x32_f16 v[8:11], v[48:51], v[68:71], v[8:11]
	v_add_u32_e32 v154, s16, v110
	s_add_i32 s44, s45, 52
	s_waitcnt lgkmcnt(5)
	v_mfma_f32_16x16x32_f16 v[84:87], v[76:79], v[56:59], v[84:87]
	s_waitcnt lgkmcnt(4)
	v_mfma_f32_16x16x32_f16 v[72:75], v[80:83], v[56:59], v[72:75]
	v_mfma_f32_16x16x32_f16 v[36:39], v[76:79], v[52:55], v[36:39]
	v_mfma_f32_16x16x32_f16 v[32:35], v[80:83], v[52:55], v[32:35]
	v_add_u32_e32 v155, s44, v98
	v_mfma_f32_16x16x32_f16 v[20:23], v[76:79], v[64:67], v[20:23]
	ds_read_b128 v[140:143], v115 offset:4096
	v_mfma_f32_16x16x32_f16 v[16:19], v[80:83], v[64:67], v[16:19]
	v_lshlrev_b32_e32 v156, 7, v155
	v_bitop3_b32 v155, v155, v99, 6 bitop3:0x6c
	v_mfma_f32_16x16x32_f16 v[4:7], v[76:79], v[68:71], v[4:7]
	ds_read_b128 v[144:147], v115 offset:6144
	v_mfma_f32_16x16x32_f16 v[0:3], v[80:83], v[68:71], v[0:3]
	v_lshl_or_b32 v114, v155, 4, v156
	v_add_u32_e32 v115, s16, v111
	s_waitcnt lgkmcnt(5)
	v_mfma_f32_16x16x32_f16 v[92:95], v[116:119], v[124:127], v[92:95]
	ds_read_b128 v[40:43], v154
	s_waitcnt lgkmcnt(5)
	v_mfma_f32_16x16x32_f16 v[88:91], v[120:123], v[124:127], v[88:91]
	s_mov_b32 m0, s43
	s_addk_i32 s13, 0x4000
	global_load_lds_dwordx4 v[150:151], off
	v_mfma_f32_16x16x32_f16 v[60:63], v[116:119], v[128:131], v[60:63]
	ds_read_b128 v[48:51], v154 offset:2048
	v_mfma_f32_16x16x32_f16 v[44:47], v[120:123], v[128:131], v[44:47]
	s_sub_i32 s44, s44, 51
	v_add_u32_e32 v155, s44, v98
	s_waitcnt lgkmcnt(5)
	v_mfma_f32_16x16x32_f16 v[28:31], v[116:119], v[132:135], v[28:31]
	ds_read_b128 v[56:59], v114
	v_mfma_f32_16x16x32_f16 v[24:27], v[120:123], v[132:135], v[24:27]
	v_lshlrev_b32_e32 v156, 7, v155
	v_bitop3_b32 v155, v155, v99, 6 bitop3:0x6c
	s_waitcnt lgkmcnt(5)
	v_mfma_f32_16x16x32_f16 v[12:15], v[116:119], v[136:139], v[12:15]
	ds_read_b128 v[52:55], v114 offset:2048
	v_mfma_f32_16x16x32_f16 v[8:11], v[120:123], v[136:139], v[8:11]
	v_lshl_or_b32 v113, v155, 4, v156
	s_waitcnt lgkmcnt(5)
	v_mfma_f32_16x16x32_f16 v[84:87], v[140:143], v[124:127], v[84:87]
	ds_read_b128 v[64:67], v113
	s_waitcnt lgkmcnt(5)
	v_mfma_f32_16x16x32_f16 v[72:75], v[144:147], v[124:127], v[72:75]
	v_mfma_f32_16x16x32_f16 v[36:39], v[140:143], v[128:131], v[36:39]
	ds_read_b128 v[68:71], v113 offset:2048
	v_mfma_f32_16x16x32_f16 v[32:35], v[144:147], v[128:131], v[32:35]
	v_mfma_f32_16x16x32_f16 v[20:23], v[140:143], v[132:135], v[20:23]
	ds_read_b128 v[76:79], v154 offset:4096
	v_mfma_f32_16x16x32_f16 v[16:19], v[144:147], v[132:135], v[16:19]
	v_mfma_f32_16x16x32_f16 v[4:7], v[140:143], v[136:139], v[4:7]
	ds_read_b128 v[80:83], v154 offset:6144
	v_mfma_f32_16x16x32_f16 v[0:3], v[144:147], v[136:139], v[0:3]
	s_waitcnt vmcnt(2)
	s_barrier
	s_waitcnt lgkmcnt(3)
	v_mfma_f32_16x16x32_f16 v[92:95], v[40:43], v[64:67], v[92:95]
	ds_read_b128 v[116:119], v115
	v_mfma_f32_16x16x32_f16 v[88:91], v[48:51], v[64:67], v[88:91]
	v_xor_b32_e32 v153, 64, v114
	s_add_i32 s4, s45, 61
	s_add_i32 s4, s4, s12
	s_lshl_b32 s4, s4, 14
	s_waitcnt lgkmcnt(3)
	v_mfma_f32_16x16x32_f16 v[60:63], v[40:43], v[68:71], v[60:63]
	ds_read_b128 v[120:123], v115 offset:2048
	v_lshl_add_u64 v[148:149], v[100:101], 0, s[4:5]
	s_and_b32 s42, s13, 0xc000
	s_add_i32 s42, s42, s27
	v_mfma_f32_16x16x32_f16 v[44:47], v[48:51], v[68:71], v[44:47]
	v_xor_b32_e32 v152, 64, v113
	s_mov_b32 m0, s42
	s_add_i32 s16, s13, 0xffff8000
	global_load_lds_dwordx4 v[148:149], off
	v_mfma_f32_16x16x32_f16 v[28:31], v[40:43], v[56:59], v[28:31]
	ds_read_b128 v[124:127], v153
	v_mfma_f32_16x16x32_f16 v[24:27], v[48:51], v[56:59], v[24:27]
	s_and_b32 s16, s16, 0xc000
	s_add_i32 s43, s42, 0x400
	v_lshl_add_u64 v[150:151], v[148:149], 0, s[8:9]
	v_mfma_f32_16x16x32_f16 v[12:15], v[40:43], v[52:55], v[12:15]
	ds_read_b128 v[128:131], v153 offset:2048
	v_mfma_f32_16x16x32_f16 v[8:11], v[48:51], v[52:55], v[8:11]
	v_add_u32_e32 v154, s16, v110
	s_add_i32 s44, s45, 103
	s_waitcnt lgkmcnt(5)
	v_mfma_f32_16x16x32_f16 v[84:87], v[76:79], v[64:67], v[84:87]
	ds_read_b128 v[132:135], v152
	s_waitcnt lgkmcnt(5)
	v_mfma_f32_16x16x32_f16 v[72:75], v[80:83], v[64:67], v[72:75]
	v_mfma_f32_16x16x32_f16 v[36:39], v[76:79], v[68:71], v[36:39]
	ds_read_b128 v[136:139], v152 offset:2048
	v_mfma_f32_16x16x32_f16 v[32:35], v[80:83], v[68:71], v[32:35]
	v_add_u32_e32 v155, s44, v98
	v_mfma_f32_16x16x32_f16 v[20:23], v[76:79], v[56:59], v[20:23]
	ds_read_b128 v[140:143], v115 offset:4096
	v_mfma_f32_16x16x32_f16 v[16:19], v[80:83], v[56:59], v[16:19]
	v_lshlrev_b32_e32 v156, 7, v155
	v_bitop3_b32 v155, v155, v99, 6 bitop3:0x6c
	v_mfma_f32_16x16x32_f16 v[4:7], v[76:79], v[52:55], v[4:7]
	ds_read_b128 v[144:147], v115 offset:6144
	v_mfma_f32_16x16x32_f16 v[0:3], v[80:83], v[52:55], v[0:3]
	v_lshl_or_b32 v114, v155, 4, v156
	v_add_u32_e32 v115, s16, v111
	s_waitcnt lgkmcnt(3)
	v_mfma_f32_16x16x32_f16 v[92:95], v[116:119], v[132:135], v[92:95]
	ds_read_b128 v[40:43], v154
	v_mfma_f32_16x16x32_f16 v[88:91], v[120:123], v[132:135], v[88:91]
	s_mov_b32 m0, s43
	s_addk_i32 s13, 0x4000
	global_load_lds_dwordx4 v[150:151], off
	s_waitcnt lgkmcnt(3)
	v_mfma_f32_16x16x32_f16 v[60:63], v[116:119], v[136:139], v[60:63]
	ds_read_b128 v[48:51], v154 offset:2048
	v_mfma_f32_16x16x32_f16 v[44:47], v[120:123], v[136:139], v[44:47]
	v_mfma_f32_16x16x32_f16 v[28:31], v[116:119], v[124:127], v[28:31]
	ds_read_b128 v[64:67], v114
	v_mfma_f32_16x16x32_f16 v[24:27], v[120:123], v[124:127], v[24:27]
	v_mfma_f32_16x16x32_f16 v[12:15], v[116:119], v[128:131], v[12:15]
	ds_read_b128 v[68:71], v114 offset:2048
	v_mfma_f32_16x16x32_f16 v[8:11], v[120:123], v[128:131], v[8:11]
	s_waitcnt lgkmcnt(5)
	v_mfma_f32_16x16x32_f16 v[84:87], v[140:143], v[132:135], v[84:87]
	s_waitcnt lgkmcnt(4)
	v_mfma_f32_16x16x32_f16 v[72:75], v[144:147], v[132:135], v[72:75]
	v_mfma_f32_16x16x32_f16 v[36:39], v[140:143], v[136:139], v[36:39]
	v_mfma_f32_16x16x32_f16 v[32:35], v[144:147], v[136:139], v[32:35]
	v_mfma_f32_16x16x32_f16 v[20:23], v[140:143], v[124:127], v[20:23]
	ds_read_b128 v[76:79], v154 offset:4096
	v_mfma_f32_16x16x32_f16 v[16:19], v[144:147], v[124:127], v[16:19]
	v_mfma_f32_16x16x32_f16 v[4:7], v[140:143], v[128:131], v[4:7]
	ds_read_b128 v[80:83], v154 offset:6144
	v_mfma_f32_16x16x32_f16 v[0:3], v[144:147], v[128:131], v[0:3]
	s_waitcnt vmcnt(2)
	s_barrier
	s_waitcnt lgkmcnt(5)
	v_mfma_f32_16x16x32_f16 v[92:95], v[40:43], v[56:59], v[92:95]
	ds_read_b128 v[116:119], v115
	s_waitcnt lgkmcnt(5)
	v_mfma_f32_16x16x32_f16 v[88:91], v[48:51], v[56:59], v[88:91]
	v_xor_b32_e32 v153, 64, v114
	s_add_i32 s4, s45, 81
	s_add_i32 s4, s4, s12
	s_lshl_b32 s4, s4, 14
	v_mfma_f32_16x16x32_f16 v[60:63], v[40:43], v[52:55], v[60:63]
	ds_read_b128 v[120:123], v115 offset:2048
	v_lshl_add_u64 v[148:149], v[100:101], 0, s[4:5]
	s_and_b32 s42, s13, 0xc000
	s_add_i32 s42, s42, s27
	v_mfma_f32_16x16x32_f16 v[44:47], v[48:51], v[52:55], v[44:47]
	s_mov_b32 m0, s42
	s_add_i32 s16, s13, 0xffff8000
	global_load_lds_dwordx4 v[148:149], off
	s_waitcnt lgkmcnt(5)
	v_mfma_f32_16x16x32_f16 v[28:31], v[40:43], v[64:67], v[28:31]
	ds_read_b128 v[132:135], v153
	v_mfma_f32_16x16x32_f16 v[24:27], v[48:51], v[64:67], v[24:27]
	s_and_b32 s16, s16, 0xc000
	s_add_i32 s43, s42, 0x400
	v_lshl_add_u64 v[150:151], v[148:149], 0, s[8:9]
	s_waitcnt lgkmcnt(5)
	v_mfma_f32_16x16x32_f16 v[12:15], v[40:43], v[68:71], v[12:15]
	ds_read_b128 v[136:139], v153 offset:2048
	v_mfma_f32_16x16x32_f16 v[8:11], v[48:51], v[68:71], v[8:11]
	v_add_u32_e32 v154, s16, v110
	s_add_i32 s44, s45, 154
	s_waitcnt lgkmcnt(5)
	v_mfma_f32_16x16x32_f16 v[84:87], v[76:79], v[56:59], v[84:87]
	s_waitcnt lgkmcnt(4)
	v_mfma_f32_16x16x32_f16 v[72:75], v[80:83], v[56:59], v[72:75]
	v_mfma_f32_16x16x32_f16 v[36:39], v[76:79], v[52:55], v[36:39]
	v_mfma_f32_16x16x32_f16 v[32:35], v[80:83], v[52:55], v[32:35]
	v_add_u32_e32 v155, s44, v98
	v_mfma_f32_16x16x32_f16 v[20:23], v[76:79], v[64:67], v[20:23]
	ds_read_b128 v[140:143], v115 offset:4096
	v_mfma_f32_16x16x32_f16 v[16:19], v[80:83], v[64:67], v[16:19]
	v_lshlrev_b32_e32 v156, 7, v155
	v_bitop3_b32 v155, v155, v99, 6 bitop3:0x6c
	v_mfma_f32_16x16x32_f16 v[4:7], v[76:79], v[68:71], v[4:7]
	ds_read_b128 v[144:147], v115 offset:6144
	v_mfma_f32_16x16x32_f16 v[0:3], v[80:83], v[68:71], v[0:3]
	v_lshl_or_b32 v114, v155, 4, v156
	v_add_u32_e32 v115, s16, v111
	s_waitcnt lgkmcnt(5)
	v_mfma_f32_16x16x32_f16 v[92:95], v[116:119], v[124:127], v[92:95]
	ds_read_b128 v[40:43], v154
	s_waitcnt lgkmcnt(5)
	v_mfma_f32_16x16x32_f16 v[88:91], v[120:123], v[124:127], v[88:91]
	s_mov_b32 m0, s43
	s_addk_i32 s13, 0x4000
	global_load_lds_dwordx4 v[150:151], off
	v_mfma_f32_16x16x32_f16 v[60:63], v[116:119], v[128:131], v[60:63]
	ds_read_b128 v[48:51], v154 offset:2048
	v_mfma_f32_16x16x32_f16 v[44:47], v[120:123], v[128:131], v[44:47]
	s_waitcnt lgkmcnt(5)
	v_mfma_f32_16x16x32_f16 v[28:31], v[116:119], v[132:135], v[28:31]
	ds_read_b128 v[56:59], v114
	v_mfma_f32_16x16x32_f16 v[24:27], v[120:123], v[132:135], v[24:27]
	s_waitcnt lgkmcnt(5)
	v_mfma_f32_16x16x32_f16 v[12:15], v[116:119], v[136:139], v[12:15]
	ds_read_b128 v[52:55], v114 offset:2048
	v_mfma_f32_16x16x32_f16 v[8:11], v[120:123], v[136:139], v[8:11]
	s_waitcnt lgkmcnt(5)
	v_mfma_f32_16x16x32_f16 v[84:87], v[140:143], v[124:127], v[84:87]
	s_waitcnt lgkmcnt(4)
	v_mfma_f32_16x16x32_f16 v[72:75], v[144:147], v[124:127], v[72:75]
	v_mfma_f32_16x16x32_f16 v[36:39], v[140:143], v[128:131], v[36:39]
	v_mfma_f32_16x16x32_f16 v[32:35], v[144:147], v[128:131], v[32:35]
	v_mfma_f32_16x16x32_f16 v[20:23], v[140:143], v[132:135], v[20:23]
	ds_read_b128 v[76:79], v154 offset:4096
	v_mfma_f32_16x16x32_f16 v[16:19], v[144:147], v[132:135], v[16:19]
	v_mfma_f32_16x16x32_f16 v[4:7], v[140:143], v[136:139], v[4:7]
	ds_read_b128 v[80:83], v154 offset:6144
	v_mfma_f32_16x16x32_f16 v[0:3], v[144:147], v[136:139], v[0:3]
	s_waitcnt vmcnt(2)
	s_barrier
	s_waitcnt lgkmcnt(5)
	v_mfma_f32_16x16x32_f16 v[92:95], v[40:43], v[64:67], v[92:95]
	ds_read_b128 v[116:119], v115
	s_waitcnt lgkmcnt(5)
	v_mfma_f32_16x16x32_f16 v[88:91], v[48:51], v[64:67], v[88:91]
	v_xor_b32_e32 v153, 64, v114
	s_add_i32 s4, s45, 2
	s_add_i32 s4, s4, s12
	s_lshl_b32 s4, s4, 14
	v_mfma_f32_16x16x32_f16 v[60:63], v[40:43], v[68:71], v[60:63]
	ds_read_b128 v[120:123], v115 offset:2048
	v_lshl_add_u64 v[148:149], v[100:101], 0, s[4:5]
	s_and_b32 s42, s13, 0xc000
	s_add_i32 s42, s42, s27
	v_mfma_f32_16x16x32_f16 v[44:47], v[48:51], v[68:71], v[44:47]
	s_mov_b32 m0, s42
	s_add_i32 s16, s13, 0xffff8000
	global_load_lds_dwordx4 v[148:149], off
	s_waitcnt lgkmcnt(5)
	v_mfma_f32_16x16x32_f16 v[28:31], v[40:43], v[56:59], v[28:31]
	ds_read_b128 v[124:127], v153
	v_mfma_f32_16x16x32_f16 v[24:27], v[48:51], v[56:59], v[24:27]
	s_and_b32 s16, s16, 0xc000
	s_add_i32 s43, s42, 0x400
	v_lshl_add_u64 v[150:151], v[148:149], 0, s[8:9]
	s_waitcnt lgkmcnt(5)
	v_mfma_f32_16x16x32_f16 v[12:15], v[40:43], v[52:55], v[12:15]
	ds_read_b128 v[128:131], v153 offset:2048
	v_mfma_f32_16x16x32_f16 v[8:11], v[48:51], v[52:55], v[8:11]
	v_add_u32_e32 v154, s16, v110
	s_add_i32 s44, s45, 205
	s_waitcnt lgkmcnt(5)
	v_mfma_f32_16x16x32_f16 v[84:87], v[76:79], v[64:67], v[84:87]
	s_waitcnt lgkmcnt(4)
	v_mfma_f32_16x16x32_f16 v[72:75], v[80:83], v[64:67], v[72:75]
	v_mfma_f32_16x16x32_f16 v[36:39], v[76:79], v[68:71], v[36:39]
	v_mfma_f32_16x16x32_f16 v[32:35], v[80:83], v[68:71], v[32:35]
	v_add_u32_e32 v155, s44, v98
	v_mfma_f32_16x16x32_f16 v[20:23], v[76:79], v[56:59], v[20:23]
	ds_read_b128 v[140:143], v115 offset:4096
	v_mfma_f32_16x16x32_f16 v[16:19], v[80:83], v[56:59], v[16:19]
	v_lshlrev_b32_e32 v156, 7, v155
	v_bitop3_b32 v155, v155, v99, 6 bitop3:0x6c
	v_mfma_f32_16x16x32_f16 v[4:7], v[76:79], v[52:55], v[4:7]
	ds_read_b128 v[144:147], v115 offset:6144
	v_mfma_f32_16x16x32_f16 v[0:3], v[80:83], v[52:55], v[0:3]
	v_lshl_or_b32 v114, v155, 4, v156
	v_add_u32_e32 v115, s16, v111
	s_waitcnt lgkmcnt(5)
	v_mfma_f32_16x16x32_f16 v[92:95], v[116:119], v[132:135], v[92:95]
	ds_read_b128 v[40:43], v154
	s_waitcnt lgkmcnt(5)
	v_mfma_f32_16x16x32_f16 v[88:91], v[120:123], v[132:135], v[88:91]
	s_mov_b32 m0, s43
	s_addk_i32 s13, 0x4000
	global_load_lds_dwordx4 v[150:151], off
	v_mfma_f32_16x16x32_f16 v[60:63], v[116:119], v[136:139], v[60:63]
	ds_read_b128 v[48:51], v154 offset:2048
	v_mfma_f32_16x16x32_f16 v[44:47], v[120:123], v[136:139], v[44:47]
	s_waitcnt lgkmcnt(5)
	v_mfma_f32_16x16x32_f16 v[28:31], v[116:119], v[124:127], v[28:31]
	ds_read_b128 v[64:67], v114
	v_mfma_f32_16x16x32_f16 v[24:27], v[120:123], v[124:127], v[24:27]
	s_waitcnt lgkmcnt(5)
	v_mfma_f32_16x16x32_f16 v[12:15], v[116:119], v[128:131], v[12:15]
	ds_read_b128 v[68:71], v114 offset:2048
	v_mfma_f32_16x16x32_f16 v[8:11], v[120:123], v[128:131], v[8:11]
	s_waitcnt lgkmcnt(5)
	v_mfma_f32_16x16x32_f16 v[84:87], v[140:143], v[132:135], v[84:87]
	s_waitcnt lgkmcnt(4)
	v_mfma_f32_16x16x32_f16 v[72:75], v[144:147], v[132:135], v[72:75]
	v_mfma_f32_16x16x32_f16 v[36:39], v[140:143], v[136:139], v[36:39]
	v_mfma_f32_16x16x32_f16 v[32:35], v[144:147], v[136:139], v[32:35]
	v_mfma_f32_16x16x32_f16 v[20:23], v[140:143], v[124:127], v[20:23]
	ds_read_b128 v[76:79], v154 offset:4096
	v_mfma_f32_16x16x32_f16 v[16:19], v[144:147], v[124:127], v[16:19]
	v_mfma_f32_16x16x32_f16 v[4:7], v[140:143], v[128:131], v[4:7]
	ds_read_b128 v[80:83], v154 offset:6144
	v_mfma_f32_16x16x32_f16 v[0:3], v[144:147], v[128:131], v[0:3]
	s_waitcnt vmcnt(2)
	s_barrier
	s_waitcnt lgkmcnt(5)
	v_mfma_f32_16x16x32_f16 v[92:95], v[40:43], v[56:59], v[92:95]
	ds_read_b128 v[116:119], v115
	s_waitcnt lgkmcnt(5)
	v_mfma_f32_16x16x32_f16 v[88:91], v[48:51], v[56:59], v[88:91]
	v_xor_b32_e32 v153, 64, v114
	s_add_i32 s4, s45, 22
	s_add_i32 s4, s4, s12
	s_lshl_b32 s4, s4, 14
	v_mfma_f32_16x16x32_f16 v[60:63], v[40:43], v[52:55], v[60:63]
	ds_read_b128 v[120:123], v115 offset:2048
	v_lshl_add_u64 v[148:149], v[100:101], 0, s[4:5]
	s_and_b32 s42, s13, 0xc000
	s_add_i32 s42, s42, s27
	v_mfma_f32_16x16x32_f16 v[44:47], v[48:51], v[52:55], v[44:47]
	s_mov_b32 m0, s42
	s_add_i32 s16, s13, 0xffff8000
	global_load_lds_dwordx4 v[148:149], off
	s_waitcnt lgkmcnt(5)
	v_mfma_f32_16x16x32_f16 v[28:31], v[40:43], v[64:67], v[28:31]
	ds_read_b128 v[132:135], v153
	v_mfma_f32_16x16x32_f16 v[24:27], v[48:51], v[64:67], v[24:27]
	s_and_b32 s16, s16, 0xc000
	s_add_i32 s43, s42, 0x400
	v_lshl_add_u64 v[150:151], v[148:149], 0, s[8:9]
	s_waitcnt lgkmcnt(5)
	v_mfma_f32_16x16x32_f16 v[12:15], v[40:43], v[68:71], v[12:15]
	ds_read_b128 v[136:139], v153 offset:2048
	v_mfma_f32_16x16x32_f16 v[8:11], v[48:51], v[68:71], v[8:11]
	v_add_u32_e32 v154, s16, v110
	s_add_i32 s44, s45, 256
	s_waitcnt lgkmcnt(5)
	v_mfma_f32_16x16x32_f16 v[84:87], v[76:79], v[56:59], v[84:87]
	s_waitcnt lgkmcnt(4)
	v_mfma_f32_16x16x32_f16 v[72:75], v[80:83], v[56:59], v[72:75]
	v_mfma_f32_16x16x32_f16 v[36:39], v[76:79], v[52:55], v[36:39]
	v_mfma_f32_16x16x32_f16 v[32:35], v[80:83], v[52:55], v[32:35]
	v_add_u32_e32 v155, s44, v98
	v_mfma_f32_16x16x32_f16 v[20:23], v[76:79], v[64:67], v[20:23]
	ds_read_b128 v[140:143], v115 offset:4096
	v_mfma_f32_16x16x32_f16 v[16:19], v[80:83], v[64:67], v[16:19]
	v_lshlrev_b32_e32 v156, 7, v155
	v_bitop3_b32 v155, v155, v99, 6 bitop3:0x6c
	v_mfma_f32_16x16x32_f16 v[4:7], v[76:79], v[68:71], v[4:7]
	ds_read_b128 v[144:147], v115 offset:6144
	v_mfma_f32_16x16x32_f16 v[0:3], v[80:83], v[68:71], v[0:3]
	v_lshl_or_b32 v114, v155, 4, v156
	v_add_u32_e32 v115, s16, v111
	s_waitcnt lgkmcnt(5)
	v_mfma_f32_16x16x32_f16 v[92:95], v[116:119], v[124:127], v[92:95]
	ds_read_b128 v[40:43], v154
	s_waitcnt lgkmcnt(5)
	v_mfma_f32_16x16x32_f16 v[88:91], v[120:123], v[124:127], v[88:91]
	s_mov_b32 m0, s43
	s_addk_i32 s13, 0x4000
	global_load_lds_dwordx4 v[150:151], off
	v_mfma_f32_16x16x32_f16 v[60:63], v[116:119], v[128:131], v[60:63]
	ds_read_b128 v[48:51], v154 offset:2048
	v_mfma_f32_16x16x32_f16 v[44:47], v[120:123], v[128:131], v[44:47]
	s_waitcnt lgkmcnt(5)
	v_mfma_f32_16x16x32_f16 v[28:31], v[116:119], v[132:135], v[28:31]
	ds_read_b128 v[56:59], v114
	v_mfma_f32_16x16x32_f16 v[24:27], v[120:123], v[132:135], v[24:27]
	s_waitcnt lgkmcnt(5)
	v_mfma_f32_16x16x32_f16 v[12:15], v[116:119], v[136:139], v[12:15]
	ds_read_b128 v[52:55], v114 offset:2048
	v_mfma_f32_16x16x32_f16 v[8:11], v[120:123], v[136:139], v[8:11]
	s_waitcnt lgkmcnt(5)
	v_mfma_f32_16x16x32_f16 v[84:87], v[140:143], v[124:127], v[84:87]
	s_waitcnt lgkmcnt(4)
	v_mfma_f32_16x16x32_f16 v[72:75], v[144:147], v[124:127], v[72:75]
	v_mfma_f32_16x16x32_f16 v[36:39], v[140:143], v[128:131], v[36:39]
	v_mfma_f32_16x16x32_f16 v[32:35], v[144:147], v[128:131], v[32:35]
	v_mfma_f32_16x16x32_f16 v[20:23], v[140:143], v[132:135], v[20:23]
	ds_read_b128 v[76:79], v154 offset:4096
	v_mfma_f32_16x16x32_f16 v[16:19], v[144:147], v[132:135], v[16:19]
	v_mfma_f32_16x16x32_f16 v[4:7], v[140:143], v[136:139], v[4:7]
	ds_read_b128 v[80:83], v154 offset:6144
	v_mfma_f32_16x16x32_f16 v[0:3], v[144:147], v[136:139], v[0:3]
	s_waitcnt vmcnt(2)
	s_barrier
	s_waitcnt lgkmcnt(5)
	v_mfma_f32_16x16x32_f16 v[92:95], v[40:43], v[64:67], v[92:95]
	ds_read_b128 v[116:119], v115
	s_waitcnt lgkmcnt(5)
	v_mfma_f32_16x16x32_f16 v[88:91], v[48:51], v[64:67], v[88:91]
	v_xor_b32_e32 v153, 64, v114
	s_add_i32 s4, s45, 42
	s_add_i32 s4, s4, s12
	s_lshl_b32 s4, s4, 14
	v_mfma_f32_16x16x32_f16 v[60:63], v[40:43], v[68:71], v[60:63]
	ds_read_b128 v[120:123], v115 offset:2048
	v_lshl_add_u64 v[148:149], v[100:101], 0, s[4:5]
	s_and_b32 s42, s13, 0xc000
	s_add_i32 s42, s42, s27
	v_mfma_f32_16x16x32_f16 v[44:47], v[48:51], v[68:71], v[44:47]
	s_mov_b32 m0, s42
	s_add_i32 s16, s13, 0xffff8000
	global_load_lds_dwordx4 v[148:149], off
	s_waitcnt lgkmcnt(5)
	v_mfma_f32_16x16x32_f16 v[28:31], v[40:43], v[56:59], v[28:31]
	ds_read_b128 v[124:127], v153
	v_mfma_f32_16x16x32_f16 v[24:27], v[48:51], v[56:59], v[24:27]
	s_and_b32 s16, s16, 0xc000
	s_add_i32 s43, s42, 0x400
	v_lshl_add_u64 v[150:151], v[148:149], 0, s[8:9]
	s_waitcnt lgkmcnt(5)
	v_mfma_f32_16x16x32_f16 v[12:15], v[40:43], v[52:55], v[12:15]
	ds_read_b128 v[128:131], v153 offset:2048
	v_mfma_f32_16x16x32_f16 v[8:11], v[48:51], v[52:55], v[8:11]
	v_add_u32_e32 v154, s16, v110
	s_add_i32 s44, s45, 53
	s_waitcnt lgkmcnt(5)
	v_mfma_f32_16x16x32_f16 v[84:87], v[76:79], v[64:67], v[84:87]
	s_waitcnt lgkmcnt(4)
	v_mfma_f32_16x16x32_f16 v[72:75], v[80:83], v[64:67], v[72:75]
	v_mfma_f32_16x16x32_f16 v[36:39], v[76:79], v[68:71], v[36:39]
	v_mfma_f32_16x16x32_f16 v[32:35], v[80:83], v[68:71], v[32:35]
	v_add_u32_e32 v155, s44, v98
	v_mfma_f32_16x16x32_f16 v[20:23], v[76:79], v[56:59], v[20:23]
	ds_read_b128 v[140:143], v115 offset:4096
	v_mfma_f32_16x16x32_f16 v[16:19], v[80:83], v[56:59], v[16:19]
	v_lshlrev_b32_e32 v156, 7, v155
	v_bitop3_b32 v155, v155, v99, 6 bitop3:0x6c
	v_mfma_f32_16x16x32_f16 v[4:7], v[76:79], v[52:55], v[4:7]
	ds_read_b128 v[144:147], v115 offset:6144
	v_mfma_f32_16x16x32_f16 v[0:3], v[80:83], v[52:55], v[0:3]
	v_lshl_or_b32 v114, v155, 4, v156
	v_add_u32_e32 v115, s16, v111
	s_waitcnt lgkmcnt(5)
	v_mfma_f32_16x16x32_f16 v[92:95], v[116:119], v[132:135], v[92:95]
	ds_read_b128 v[40:43], v154
	s_waitcnt lgkmcnt(5)
	v_mfma_f32_16x16x32_f16 v[88:91], v[120:123], v[132:135], v[88:91]
	s_mov_b32 m0, s43
	s_addk_i32 s13, 0x4000
	global_load_lds_dwordx4 v[150:151], off
	v_mfma_f32_16x16x32_f16 v[60:63], v[116:119], v[136:139], v[60:63]
	ds_read_b128 v[48:51], v154 offset:2048
	v_mfma_f32_16x16x32_f16 v[44:47], v[120:123], v[136:139], v[44:47]
	s_sub_i32 s44, s44, 51
	v_add_u32_e32 v155, s44, v98
	s_waitcnt lgkmcnt(5)
	v_mfma_f32_16x16x32_f16 v[28:31], v[116:119], v[124:127], v[28:31]
	ds_read_b128 v[64:67], v114
	v_mfma_f32_16x16x32_f16 v[24:27], v[120:123], v[124:127], v[24:27]
	v_lshlrev_b32_e32 v156, 7, v155
	v_bitop3_b32 v155, v155, v99, 6 bitop3:0x6c
	s_waitcnt lgkmcnt(5)
	v_mfma_f32_16x16x32_f16 v[12:15], v[116:119], v[128:131], v[12:15]
	ds_read_b128 v[68:71], v114 offset:2048
	v_mfma_f32_16x16x32_f16 v[8:11], v[120:123], v[128:131], v[8:11]
	v_lshl_or_b32 v113, v155, 4, v156
	s_waitcnt lgkmcnt(5)
	v_mfma_f32_16x16x32_f16 v[84:87], v[140:143], v[132:135], v[84:87]
	ds_read_b128 v[56:59], v113
	s_waitcnt lgkmcnt(5)
	v_mfma_f32_16x16x32_f16 v[72:75], v[144:147], v[132:135], v[72:75]
	v_mfma_f32_16x16x32_f16 v[36:39], v[140:143], v[136:139], v[36:39]
	ds_read_b128 v[52:55], v113 offset:2048
	v_mfma_f32_16x16x32_f16 v[32:35], v[144:147], v[136:139], v[32:35]
	v_mfma_f32_16x16x32_f16 v[20:23], v[140:143], v[124:127], v[20:23]
	ds_read_b128 v[76:79], v154 offset:4096
	v_mfma_f32_16x16x32_f16 v[16:19], v[144:147], v[124:127], v[16:19]
	s_add_i32 s45, s45, 2
	s_add_i32 s14, s14, 1
	v_mfma_f32_16x16x32_f16 v[4:7], v[140:143], v[128:131], v[4:7]
	ds_read_b128 v[80:83], v154 offset:6144
	s_cmp_eq_u32 s14, 10
	v_mfma_f32_16x16x32_f16 v[0:3], v[144:147], v[128:131], v[0:3]
	s_cbranch_scc0 .Lc1_loop
	s_waitcnt vmcnt(0) lgkmcnt(0)
	s_cmpk_gt_u32 s34, 0x1ff
	s_barrier
	s_cbranch_scc1 .LBB3_8
	s_load_dword s0, s[0:1], 0x38
	v_lshl_or_b32 v40, s10, 6, v96
	s_movk_i32 s4, 0x110
	v_lshlrev_b32_e32 v41, 3, v99
	s_lshl_b32 s1, s11, 1
	v_mul_lo_u32 v40, v40, s4
	v_add3_u32 v48, s1, v41, v40
	v_mov_b32_e32 v40, v93
	v_mov_b32_e32 v41, v94
	s_waitcnt lgkmcnt(0)
	v_pk_mul_f32 v[40:41], s[0:1], v[40:41] op_sel_hi:[0,1]
	v_fma_mixlo_f16 v42, s0, v92, 0
	v_cvt_pk_f16_f32 v41, v40, v41
	v_pack_b32_f16 v40, v42, v41
	v_fma_mixlo_f16 v42, s0, v95, 0
	v_alignbit_b32 v41, v42, v41, 16
	v_mov_b32_e32 v42, v89
	v_mov_b32_e32 v43, v90
	v_pk_mul_f32 v[42:43], s[0:1], v[42:43] op_sel_hi:[0,1]
	v_fma_mixlo_f16 v49, s0, v88, 0
	v_cvt_pk_f16_f32 v43, v42, v43
	v_pack_b32_f16 v42, v49, v43
	v_fma_mixlo_f16 v49, s0, v91, 0
	v_alignbit_b32 v43, v49, v43, 16
	ds_write2_b64 v48, v[40:41], v[42:43] offset1:4
	v_mov_b32_e32 v40, v85
	v_mov_b32_e32 v41, v86
	v_pk_mul_f32 v[40:41], s[0:1], v[40:41] op_sel_hi:[0,1]
	v_fma_mixlo_f16 v42, s0, v84, 0
	v_cvt_pk_f16_f32 v41, v40, v41
	v_pack_b32_f16 v40, v42, v41
	v_fma_mixlo_f16 v42, s0, v87, 0
	v_alignbit_b32 v41, v42, v41, 16
	v_mov_b32_e32 v42, v73
	v_mov_b32_e32 v43, v74
	v_pk_mul_f32 v[42:43], s[0:1], v[42:43] op_sel_hi:[0,1]
	v_fma_mixlo_f16 v49, s0, v72, 0
	v_cvt_pk_f16_f32 v43, v42, v43
	v_pack_b32_f16 v42, v49, v43
	v_fma_mixlo_f16 v49, s0, v75, 0
	v_alignbit_b32 v43, v49, v43, 16
	ds_write2_b64 v48, v[40:41], v[42:43] offset0:8 offset1:12
	v_mov_b32_e32 v40, v61
	v_mov_b32_e32 v41, v62
	v_pk_mul_f32 v[40:41], s[0:1], v[40:41] op_sel_hi:[0,1]
	v_fma_mixlo_f16 v42, s0, v60, 0
	v_cvt_pk_f16_f32 v41, v40, v41
	v_pack_b32_f16 v40, v42, v41
	v_fma_mixlo_f16 v42, s0, v63, 0
	v_alignbit_b32 v41, v42, v41, 16
	v_mov_b32_e32 v42, v45
	v_mov_b32_e32 v43, v46
	v_pk_mul_f32 v[42:43], s[0:1], v[42:43] op_sel_hi:[0,1]
	v_fma_mixlo_f16 v44, s0, v44, 0
	v_cvt_pk_f16_f32 v43, v42, v43
	v_pack_b32_f16 v42, v44, v43
	v_fma_mixlo_f16 v44, s0, v47, 0
	v_alignbit_b32 v43, v44, v43, 16
	v_add_u32_e32 v44, 0x1000, v48
	ds_write2_b64 v44, v[40:41], v[42:43] offset0:32 offset1:36
	v_fma_mixlo_f16 v40, s0, v36, 0
	v_mov_b32_e32 v36, v37
	v_mov_b32_e32 v37, v38
	v_pk_mul_f32 v[36:37], s[0:1], v[36:37] op_sel_hi:[0,1]
	v_cvt_pk_f16_f32 v37, v36, v37
	v_fma_mixlo_f16 v38, s0, v39, 0
	v_pack_b32_f16 v36, v40, v37
	v_alignbit_b32 v37, v38, v37, 16
	v_fma_mixlo_f16 v38, s0, v32, 0
	v_mov_b32_e32 v32, v33
	v_mov_b32_e32 v33, v34
	v_pk_mul_f32 v[32:33], s[0:1], v[32:33] op_sel_hi:[0,1]
	v_cvt_pk_f16_f32 v33, v32, v33
	v_fma_mixlo_f16 v34, s0, v35, 0
	v_pack_b32_f16 v32, v38, v33
	v_alignbit_b32 v33, v34, v33, 16
	ds_write2_b64 v44, v[36:37], v[32:33] offset0:40 offset1:44
	v_fma_mixlo_f16 v32, s0, v28, 0
	v_mov_b32_e32 v28, v29
	v_mov_b32_e32 v29, v30
	v_pk_mul_f32 v[28:29], s[0:1], v[28:29] op_sel_hi:[0,1]
	v_cvt_pk_f16_f32 v29, v28, v29
	v_fma_mixlo_f16 v30, s0, v31, 0
	v_pack_b32_f16 v28, v32, v29
	v_alignbit_b32 v29, v30, v29, 16
	v_fma_mixlo_f16 v30, s0, v24, 0
	v_mov_b32_e32 v24, v25
	v_mov_b32_e32 v25, v26
	v_pk_mul_f32 v[24:25], s[0:1], v[24:25] op_sel_hi:[0,1]
	v_cvt_pk_f16_f32 v25, v24, v25
	v_fma_mixlo_f16 v26, s0, v27, 0
	v_pack_b32_f16 v24, v30, v25
	v_alignbit_b32 v25, v26, v25, 16
	v_add_u32_e32 v26, 0x2000, v48
	ds_write2_b64 v26, v[28:29], v[24:25] offset0:64 offset1:68
	v_fma_mixlo_f16 v24, s0, v20, 0
	v_mov_b32_e32 v20, v21
	v_mov_b32_e32 v21, v22
	v_pk_mul_f32 v[20:21], s[0:1], v[20:21] op_sel_hi:[0,1]
	v_cvt_pk_f16_f32 v21, v20, v21
	v_fma_mixlo_f16 v22, s0, v23, 0
	v_pack_b32_f16 v20, v24, v21
	v_alignbit_b32 v21, v22, v21, 16
	v_fma_mixlo_f16 v22, s0, v16, 0
	v_mov_b32_e32 v16, v17
	v_mov_b32_e32 v17, v18
	v_pk_mul_f32 v[16:17], s[0:1], v[16:17] op_sel_hi:[0,1]
	v_cvt_pk_f16_f32 v17, v16, v17
	v_fma_mixlo_f16 v18, s0, v19, 0
	v_pack_b32_f16 v16, v22, v17
	v_alignbit_b32 v17, v18, v17, 16
	ds_write2_b64 v26, v[20:21], v[16:17] offset0:72 offset1:76
	v_fma_mixlo_f16 v16, s0, v12, 0
	v_mov_b32_e32 v12, v13
	v_mov_b32_e32 v13, v14
	v_pk_mul_f32 v[12:13], s[0:1], v[12:13] op_sel_hi:[0,1]
	v_cvt_pk_f16_f32 v13, v12, v13
	v_fma_mixlo_f16 v14, s0, v15, 0
	v_pack_b32_f16 v12, v16, v13
	v_alignbit_b32 v13, v14, v13, 16
	v_fma_mixlo_f16 v14, s0, v8, 0
	v_mov_b32_e32 v8, v9
	v_mov_b32_e32 v9, v10
	v_pk_mul_f32 v[8:9], s[0:1], v[8:9] op_sel_hi:[0,1]
	v_cvt_pk_f16_f32 v9, v8, v9
	v_fma_mixlo_f16 v10, s0, v11, 0
	v_pack_b32_f16 v8, v14, v9
	v_alignbit_b32 v9, v10, v9, 16
	v_add_u32_e32 v10, 0x3000, v48
	ds_write2_b64 v10, v[12:13], v[8:9] offset0:96 offset1:100
	v_fma_mixlo_f16 v8, s0, v4, 0
	v_mov_b32_e32 v4, v5
	v_mov_b32_e32 v5, v6
	v_pk_mul_f32 v[4:5], s[0:1], v[4:5] op_sel_hi:[0,1]
	v_cvt_pk_f16_f32 v5, v4, v5
	v_fma_mixlo_f16 v6, s0, v7, 0
	v_pack_b32_f16 v4, v8, v5
	v_alignbit_b32 v5, v6, v5, 16
	v_fma_mixlo_f16 v6, s0, v0, 0
	v_mov_b32_e32 v0, v1
	v_mov_b32_e32 v1, v2
	v_pk_mul_f32 v[0:1], s[0:1], v[0:1] op_sel_hi:[0,1]
	v_cvt_pk_f16_f32 v1, v0, v1
	v_fma_mixlo_f16 v2, s0, v3, 0
	v_pack_b32_f16 v0, v6, v1
	v_alignbit_b32 v1, v2, v1, 16
	ds_write2_b64 v10, v[4:5], v[0:1] offset0:104 offset1:108
